# v44 + canonicalising self-max folded in every attention loop (GQA, NA, peeled MLA steps): 57 more VALU removed
# baseline (speedup 1.0000x reference)
.LBB0_563:
	s_or_b64 exec, exec, s[2:3]
	v_mul_f32_e32 v0, v108, v0
	v_mul_f32_e32 v1, v108, v1
	v_mul_f32_e32 v27, v108, v27
	v_mul_f32_e32 v0, v0, v114
	v_mul_f32_e32 v1, v1, v113
	v_mul_f32_e32 v27, v27, v135
	v_med3_f32 v0, v0, s69, v203
	v_med3_f32 v1, v1, s69, v203
	v_mov_b32_e32 v135, v187
	v_cvt_pk_fp8_f32 v135, v0, v1
	v_mul_f32_e32 v2, v108, v2
	v_mul_f32_e32 v3, v108, v3
	v_mul_f32_e32 v2, v2, v112
	v_mul_f32_e32 v3, v3, v111
	v_med3_f32 v0, v2, s69, v203
	v_med3_f32 v1, v3, s69, v203
	v_mul_f32_e32 v26, v108, v26
	v_cvt_pk_fp8_f32 v135, v0, v1 op_sel:[0,0,1]
	v_max_f32_e32 v0, v106, v106
	v_max_f32_e32 v1, v107, v107
	v_mul_f32_e32 v26, v26, v136
	v_med3_f32 v0, v0, s69, v203
	v_med3_f32 v1, v1, s69, v203
	v_mov_b32_e32 v136, v187
	v_cvt_pk_fp8_f32 v136, v0, v1
	v_max_f32_e32 v2, v102, v102
	v_max_f32_e32 v1, v103, v103
	v_med3_f32 v0, v2, s69, v203
	v_med3_f32 v1, v1, s69, v203
	v_mul_f32_e32 v25, v108, v25
	v_cvt_pk_fp8_f32 v136, v0, v1 op_sel:[0,0,1]
	v_max_f32_e32 v0, v100, v100
	v_max_f32_e32 v1, v101, v101
	v_mul_f32_e32 v25, v25, v137
	v_med3_f32 v0, v0, s69, v203
	v_med3_f32 v1, v1, s69, v203
	v_mov_b32_e32 v137, v187
	v_cvt_pk_fp8_f32 v137, v0, v1
	v_max_f32_e32 v2, v98, v98
	v_max_f32_e32 v1, v99, v99
	v_med3_f32 v0, v2, s69, v203
	v_med3_f32 v1, v1, s69, v203
	v_mul_f32_e32 v24, v108, v24
	v_cvt_pk_fp8_f32 v137, v0, v1 op_sel:[0,0,1]
	v_max_f32_e32 v0, v96, v96
	v_max_f32_e32 v1, v97, v97
	v_mul_f32_e32 v24, v24, v138
	v_med3_f32 v0, v0, s69, v203
	v_med3_f32 v1, v1, s69, v203
	v_mov_b32_e32 v138, v187
	v_cvt_pk_fp8_f32 v138, v0, v1
	v_max_f32_e32 v2, v94, v94
	v_max_f32_e32 v1, v95, v95
	v_med3_f32 v0, v2, s69, v203
	v_med3_f32 v1, v1, s69, v203
	v_mul_f32_e32 v31, v108, v31
	v_cvt_pk_fp8_f32 v138, v0, v1 op_sel:[0,0,1]
	v_max_f32_e32 v0, v92, v92
	v_max_f32_e32 v1, v93, v93
	v_mul_f32_e32 v31, v31, v139
	v_med3_f32 v0, v0, s69, v203
	v_med3_f32 v1, v1, s69, v203
	v_mov_b32_e32 v139, v187
	v_cvt_pk_fp8_f32 v139, v0, v1
	v_max_f32_e32 v2, v90, v90
	v_max_f32_e32 v1, v91, v91
	v_med3_f32 v0, v2, s69, v203
	v_med3_f32 v1, v1, s69, v203
	v_mul_f32_e32 v30, v108, v30
	v_cvt_pk_fp8_f32 v139, v0, v1 op_sel:[0,0,1]
	v_max_f32_e32 v0, v88, v88
	v_max_f32_e32 v1, v89, v89
	v_mul_f32_e32 v30, v30, v140
	v_med3_f32 v0, v0, s69, v203
	v_med3_f32 v1, v1, s69, v203
	v_mov_b32_e32 v140, v187
	v_cvt_pk_fp8_f32 v140, v0, v1
	v_max_f32_e32 v2, v86, v86
	v_max_f32_e32 v1, v87, v87
	v_med3_f32 v0, v2, s69, v203
	v_med3_f32 v1, v1, s69, v203
	v_mul_f32_e32 v29, v108, v29
	v_cvt_pk_fp8_f32 v140, v0, v1 op_sel:[0,0,1]
	v_max_f32_e32 v0, v84, v84
	v_max_f32_e32 v1, v85, v85
	v_mul_f32_e32 v29, v29, v141
	v_med3_f32 v0, v0, s69, v203
	v_med3_f32 v1, v1, s69, v203
	v_mov_b32_e32 v141, v187
	v_cvt_pk_fp8_f32 v141, v0, v1
	v_max_f32_e32 v2, v82, v82
	v_max_f32_e32 v1, v83, v83
	v_med3_f32 v0, v2, s69, v203
	v_med3_f32 v1, v1, s69, v203
	v_mul_f32_e32 v28, v108, v28
	v_cvt_pk_fp8_f32 v141, v0, v1 op_sel:[0,0,1]
	v_max_f32_e32 v0, v80, v80
	v_max_f32_e32 v1, v81, v81
	v_mul_f32_e32 v28, v28, v142
	v_med3_f32 v0, v0, s69, v203
	v_med3_f32 v1, v1, s69, v203
	v_mov_b32_e32 v142, v187
	v_cvt_pk_fp8_f32 v142, v0, v1
	v_mul_f32_e32 v4, v108, v4
	v_mul_f32_e32 v5, v108, v5
	v_mul_f32_e32 v60, v60, v108
	v_mul_f32_e32 v61, v61, v108
	v_mul_f32_e32 v56, v56, v108
	v_mul_f32_e32 v57, v57, v108
	v_mul_f32_e32 v52, v52, v108
	v_mul_f32_e32 v53, v108, v53
	v_mul_f32_e32 v48, v108, v48
	v_mul_f32_e32 v49, v108, v49
	v_mul_f32_e32 v44, v108, v44
	v_mul_f32_e32 v45, v108, v45
	v_mul_f32_e32 v40, v108, v40
	v_mul_f32_e32 v41, v108, v41
	v_mul_f32_e32 v36, v108, v36
	v_mul_f32_e32 v37, v108, v37
	v_mul_f32_e32 v32, v108, v32
	v_mul_f32_e32 v33, v108, v33
	v_mul_f32_e32 v20, v108, v20
	v_mul_f32_e32 v4, v4, v118
	v_mul_f32_e32 v5, v5, v117
	v_max_f32_e32 v2, v78, v78
	v_max_f32_e32 v1, v79, v79
	v_mul_f32_e32 v60, v60, v182
	v_mul_f32_e32 v61, v61, v181
	v_mul_f32_e32 v56, v56, v178
	v_mul_f32_e32 v57, v57, v177
	v_mul_f32_e32 v52, v52, v174
	v_mul_f32_e32 v53, v53, v173
	v_mul_f32_e32 v48, v48, v162
	v_mul_f32_e32 v49, v49, v161
	v_mul_f32_e32 v44, v44, v158
	v_mul_f32_e32 v45, v45, v157
	v_mul_f32_e32 v40, v40, v154
	v_mul_f32_e32 v41, v41, v153
	v_mul_f32_e32 v36, v36, v150
	v_mul_f32_e32 v37, v37, v149
	v_mul_f32_e32 v32, v32, v146
	v_mul_f32_e32 v33, v33, v145
	v_mul_f32_e32 v20, v20, v134
	v_mul_f32_e32 v19, v108, v19
	v_mul_f32_e32 v12, v108, v12
	v_mul_f32_e32 v13, v108, v13
	v_mul_f32_e32 v14, v108, v14
	v_mul_f32_e32 v15, v108, v15
	v_mul_f32_e32 v8, v108, v8
	v_mul_f32_e32 v9, v108, v9
	v_mul_f32_e32 v10, v108, v10
	v_med3_f32 v4, v4, s69, v203
	v_med3_f32 v5, v5, s69, v203
	v_mov_b32_e32 v134, v187
	v_med3_f32 v0, v2, s69, v203
	v_med3_f32 v1, v1, s69, v203
	v_mul_f32_e32 v35, v108, v35
	v_mul_f32_e32 v21, v108, v21
	v_mul_f32_e32 v19, v19, v127
	v_mul_f32_e32 v12, v12, v126
	v_mul_f32_e32 v13, v13, v125
	v_mul_f32_e32 v14, v14, v124
	v_mul_f32_e32 v15, v15, v123
	v_mul_f32_e32 v8, v8, v122
	v_mul_f32_e32 v9, v9, v121
	v_mul_f32_e32 v10, v10, v120
	v_med3_f32 v60, v60, s69, v203
	v_med3_f32 v61, v61, s69, v203
	v_mov_b32_e32 v120, v187
	v_med3_f32 v56, v56, s69, v203
	v_med3_f32 v57, v57, s69, v203
	v_mov_b32_e32 v121, v187
	v_med3_f32 v52, v52, s69, v203
	v_med3_f32 v53, v53, s69, v203
	v_mov_b32_e32 v122, v187
	v_med3_f32 v48, v48, s69, v203
	v_med3_f32 v49, v49, s69, v203
	v_mov_b32_e32 v123, v187
	v_med3_f32 v44, v44, s69, v203
	v_med3_f32 v45, v45, s69, v203
	v_mov_b32_e32 v124, v187
	v_med3_f32 v40, v40, s69, v203
	v_med3_f32 v41, v41, s69, v203
	v_mov_b32_e32 v125, v187
	v_med3_f32 v36, v36, s69, v203
	v_med3_f32 v37, v37, s69, v203
	v_mov_b32_e32 v126, v187
	v_med3_f32 v32, v32, s69, v203
	v_med3_f32 v33, v33, s69, v203
	v_mov_b32_e32 v127, v187
	v_cvt_pk_fp8_f32 v134, v4, v5
	v_cvt_pk_fp8_f32 v142, v0, v1 op_sel:[0,0,1]
	v_max_f32_e32 v0, v76, v76
	v_max_f32_e32 v1, v77, v77
	v_mul_f32_e32 v35, v35, v143
	v_mul_f32_e32 v21, v21, v133
	v_mul_f32_e32 v6, v108, v6
	v_mul_f32_e32 v7, v108, v7
	v_cvt_pk_fp8_f32 v120, v60, v61
	v_cvt_pk_fp8_f32 v121, v56, v57
	v_cvt_pk_fp8_f32 v122, v52, v53
	v_cvt_pk_fp8_f32 v123, v48, v49
	v_cvt_pk_fp8_f32 v124, v44, v45
	v_cvt_pk_fp8_f32 v125, v40, v41
	v_cvt_pk_fp8_f32 v126, v36, v37
	v_cvt_pk_fp8_f32 v127, v32, v33
	v_med3_f32 v8, v8, s69, v203
	v_med3_f32 v9, v9, s69, v203
	v_mov_b32_e32 v133, v187
	v_med3_f32 v0, v0, s69, v203
	v_med3_f32 v1, v1, s69, v203
	v_mov_b32_e32 v143, v187
	v_mul_f32_e32 v62, v62, v108
	v_mul_f32_e32 v63, v63, v108
	v_mul_f32_e32 v58, v58, v108
	v_mul_f32_e32 v59, v59, v108
	v_mul_f32_e32 v54, v108, v54
	v_mul_f32_e32 v55, v108, v55
	v_mul_f32_e32 v50, v108, v50
	v_mul_f32_e32 v51, v108, v51
	v_mul_f32_e32 v46, v108, v46
	v_mul_f32_e32 v47, v108, v47
	v_mul_f32_e32 v42, v108, v42
	v_mul_f32_e32 v43, v108, v43
	v_mul_f32_e32 v38, v108, v38
	v_mul_f32_e32 v39, v108, v39
	v_mul_f32_e32 v34, v108, v34
	v_mul_f32_e32 v16, v108, v16
	v_mul_f32_e32 v17, v108, v17
	v_mul_f32_e32 v6, v6, v116
	v_mul_f32_e32 v7, v7, v115
	v_cvt_pk_fp8_f32 v133, v8, v9
	v_cvt_pk_fp8_f32 v143, v0, v1
	v_mul_u32_u24_e32 v0, 0xd0, v186
	s_and_b32 s3, s17, 0x3fffffc0
	v_mul_f32_e32 v62, v62, v180
	v_mul_f32_e32 v63, v63, v179
	v_mul_f32_e32 v58, v58, v176
	v_mul_f32_e32 v59, v59, v175
	v_mul_f32_e32 v54, v54, v172
	v_mul_f32_e32 v55, v55, v163
	v_mul_f32_e32 v50, v50, v160
	v_mul_f32_e32 v51, v51, v159
	v_mul_f32_e32 v46, v46, v156
	v_mul_f32_e32 v47, v47, v155
	v_mul_f32_e32 v42, v42, v152
	v_mul_f32_e32 v43, v43, v151
	v_mul_f32_e32 v38, v38, v148
	v_mul_f32_e32 v39, v39, v147
	v_mul_f32_e32 v34, v34, v144
	v_mul_f32_e32 v23, v108, v23
	v_mul_f32_e32 v16, v16, v130
	v_mul_f32_e32 v17, v17, v129
	v_mul_f32_e32 v18, v108, v18
	v_mul_f32_e32 v11, v108, v11
	v_med3_f32 v6, v6, s69, v203
	v_med3_f32 v7, v7, s69, v203
	v_add3_u32 v216, 0, v0, v72
	s_lshl_b32 s3, s3, 2
	s_ashr_i32 s18, s18, 6
	v_mul_f32_e32 v23, v23, v131
	v_mul_f32_e32 v18, v18, v128
	v_mul_f32_e32 v11, v11, v119
	v_med3_f32 v62, v62, s69, v203
	v_med3_f32 v63, v63, s69, v203
	v_med3_f32 v56, v58, s69, v203
	v_med3_f32 v57, v59, s69, v203
	v_med3_f32 v54, v54, s69, v203
	v_med3_f32 v55, v55, s69, v203
	v_med3_f32 v48, v50, s69, v203
	v_med3_f32 v49, v51, s69, v203
	v_med3_f32 v46, v46, s69, v203
	v_med3_f32 v47, v47, s69, v203
	v_med3_f32 v40, v42, s69, v203
	v_med3_f32 v41, v43, s69, v203
	v_med3_f32 v38, v38, s69, v203
	v_med3_f32 v39, v39, s69, v203
	v_med3_f32 v32, v34, s69, v203
	v_med3_f32 v33, v35, s69, v203
	v_med3_f32 v28, v28, s69, v203
	v_med3_f32 v29, v29, s69, v203
	v_mov_b32_e32 v128, v187
	v_med3_f32 v24, v24, s69, v203
	v_med3_f32 v25, v25, s69, v203
	v_mov_b32_e32 v129, v187
	v_med3_f32 v20, v20, s69, v203
	v_med3_f32 v21, v21, s69, v203
	v_mov_b32_e32 v130, v187
	v_med3_f32 v16, v16, s69, v203
	v_med3_f32 v17, v17, s69, v203
	v_mov_b32_e32 v131, v187
	v_cvt_pk_fp8_f32 v134, v6, v7 op_sel:[0,0,1]
	ds_read_b128 v[0:3], v216
	ds_read_b128 v[4:7], v216 offset:16
	s_add_i32 s3, s3, 0
	s_ashr_i32 s19, s18, 31
	s_lshl_b32 s2, s74, 1
	v_cvt_pk_fp8_f32 v120, v62, v63 op_sel:[0,0,1]
	v_cvt_pk_fp8_f32 v121, v56, v57 op_sel:[0,0,1]
	v_cvt_pk_fp8_f32 v122, v54, v55 op_sel:[0,0,1]
	v_cvt_pk_fp8_f32 v123, v48, v49 op_sel:[0,0,1]
	v_cvt_pk_fp8_f32 v124, v46, v47 op_sel:[0,0,1]
	v_cvt_pk_fp8_f32 v125, v40, v41 op_sel:[0,0,1]
	v_cvt_pk_fp8_f32 v126, v38, v39 op_sel:[0,0,1]
	v_cvt_pk_fp8_f32 v127, v32, v33 op_sel:[0,0,1]
	v_cvt_pk_fp8_f32 v128, v28, v29
	v_cvt_pk_fp8_f32 v129, v24, v25
	v_cvt_pk_fp8_f32 v130, v20, v21
	v_cvt_pk_fp8_f32 v131, v16, v17
	v_med3_f32 v8, v10, s69, v203
	v_med3_f32 v9, v11, s69, v203
	s_add_i32 s79, s3, 0x18000
	s_lshl_b64 s[18:19], s[18:19], 16
	v_mul_f32_e32 v22, v108, v22
	v_cvt_pk_fp8_f32 v133, v8, v9 op_sel:[0,0,1]
	v_max_f32_e32 v8, v74, v74
	v_max_f32_e32 v9, v75, v75
	s_add_u32 s18, s44, s18
	v_mul_f32_e32 v22, v22, v132
	v_med3_f32 v8, v8, s69, v203
	v_med3_f32 v9, v9, s69, v203
	s_addc_u32 s19, s45, s19
	v_med3_f32 v30, v30, s69, v203
	v_med3_f32 v31, v31, s69, v203
	v_med3_f32 v24, v26, s69, v203
	v_med3_f32 v25, v27, s69, v203
	v_med3_f32 v22, v22, s69, v203
	v_med3_f32 v23, v23, s69, v203
	v_med3_f32 v16, v18, s69, v203
	v_med3_f32 v17, v19, s69, v203
	v_cvt_pk_fp8_f32 v143, v8, v9 op_sel:[0,0,1]
	v_lshl_add_u64 v[8:9], s[18:19], 0, v[104:105]
	v_cvt_pk_fp8_f32 v128, v30, v31 op_sel:[0,0,1]
	v_cvt_pk_fp8_f32 v129, v24, v25 op_sel:[0,0,1]
	v_cvt_pk_fp8_f32 v130, v22, v23 op_sel:[0,0,1]
	v_cvt_pk_fp8_f32 v131, v16, v17 op_sel:[0,0,1]
	s_waitcnt lgkmcnt(0)
	v_mfma_scale_f32_32x32x64_f8f6f4 v[16:31], v[0:7], v[120:127], 0, v205, v205 op_sel_hi:[0,0,0]
	ds_read_b128 v[0:3], v216 offset:64
	ds_read_b128 v[4:7], v216 offset:80
	global_load_dwordx4 v[172:175], v[8:9], off
	v_med3_f32 v12, v12, s69, v203
	v_med3_f32 v13, v13, s69, v203
	v_mov_b32_e32 v132, v187
	v_cvt_pk_fp8_f32 v132, v12, v13
	v_med3_f32 v14, v14, s69, v203
	v_med3_f32 v15, v15, s69, v203
	s_mov_b32 s17, s16
	v_cvt_pk_fp8_f32 v132, v14, v15 op_sel:[0,0,1]
	s_mov_b32 s18, s16
	s_mov_b32 s19, s16
	s_mov_b32 s20, s16
	s_mov_b32 s21, s16
	s_mov_b32 s22, s16
	s_waitcnt lgkmcnt(0)
	v_mfma_scale_f32_32x32x64_f8f6f4 v[16:31], v[0:7], v[128:135], v[16:31], v205, v205 op_sel_hi:[0,0,0]
	v_sub_u32_e32 v0, v216, v73
	ds_read_b128 v[32:35], v0 offset:128
	ds_read_b128 v[36:39], v0 offset:160
	s_mov_b32 s23, s16
	s_mov_b32 s24, s16
	s_mov_b32 s25, s16
	s_mov_b32 s26, s16
	s_mov_b32 s27, s16
	s_mov_b32 s28, s16
	s_mov_b32 s29, s16
	s_mov_b32 s30, s16
	s_mov_b32 s31, s16
	v_mov_b64_e32 v[0:1], s[16:17]
	v_and_b32_e32 v64, 63, v110
	v_mov_b64_e32 v[14:15], s[30:31]
	v_mov_b64_e32 v[2:3], s[18:19]
	s_waitcnt lgkmcnt(0)
	v_mfma_scale_f32_32x32x64_f8f6f4 v[16:31], v[32:39], v[136:143], v[16:31], v205, v205 op_sel_hi:[0,0,0]
	v_mov_b64_e32 v[4:5], s[20:21]
	v_mov_b64_e32 v[6:7], s[22:23]
	v_mov_b64_e32 v[8:9], s[24:25]
	v_mov_b64_e32 v[10:11], s[26:27]
	v_mov_b64_e32 v[12:13], s[28:29]
	v_sub_u32_e32 v217, 0, v73
	v_mov_b32_e32 v112, 0x38383838
	v_mov_b64_e32 v[62:63], v[14:15]
	s_mov_b32 s78, 2
	v_lshl_add_u32 v209, v186, 2, s79
	v_mov_b32_e32 v113, v112
	v_mov_b32_e32 v114, v112
	v_mov_b32_e32 v115, v112
	v_mov_b32_e32 v116, v112
	s_nop 5
	v_max_f32_e32 v32, v16, v17
	v_max3_f32 v32, v32, v18, v19
	v_max3_f32 v32, v32, v20, v21
	v_max3_f32 v32, v32, v22, v23
	v_max3_f32 v32, v32, v24, v25
	v_max3_f32 v32, v32, v26, v27
	v_max3_f32 v32, v32, v28, v29
	v_max3_f32 v32, v32, v30, v31
	v_mov_b32_e32 v33, v32
	s_nop 1
	v_permlane32_swap_b32_e32 v32, v33
	v_max_f32_e32 v32, v32, v33
	v_fmamk_f32 v33, v32, 0x3dd53b94, v201
	v_fmamk_f32 v32, v32, 0x3dd53b94, v202
	v_max_f32_e32 v32, 0xf149f2ca, v32
	v_cmp_ge_f32_e32 vcc, s70, v33
	v_sub_f32_e32 v33, 0xf149f2ca, v32
	s_cmp_eq_u64 vcc, exec
	v_exp_f32_e32 v33, v33
	s_cselect_b64 vcc, -1, 0
	v_cndmask_b32_e32 v192, v32, v204, vcc
	v_pk_fma_f32 v[178:179], v[16:17], s[40:41], v[192:193] op_sel_hi:[1,0,0] neg_lo:[0,0,1] neg_hi:[0,0,1]
	v_mul_u32_u24_e32 v16, 0x50, v186
	v_pk_fma_f32 v[152:153], v[30:31], s[40:41], v[192:193] op_sel_hi:[1,0,0] neg_lo:[0,0,1] neg_hi:[0,0,1]
	v_pk_fma_f32 v[154:155], v[28:29], s[40:41], v[192:193] op_sel_hi:[1,0,0] neg_lo:[0,0,1] neg_hi:[0,0,1]
	v_pk_fma_f32 v[156:157], v[26:27], s[40:41], v[192:193] op_sel_hi:[1,0,0] neg_lo:[0,0,1] neg_hi:[0,0,1]
	v_pk_fma_f32 v[158:159], v[24:25], s[40:41], v[192:193] op_sel_hi:[1,0,0] neg_lo:[0,0,1] neg_hi:[0,0,1]
	v_pk_fma_f32 v[160:161], v[22:23], s[40:41], v[192:193] op_sel_hi:[1,0,0] neg_lo:[0,0,1] neg_hi:[0,0,1]
	v_pk_fma_f32 v[162:163], v[20:21], s[40:41], v[192:193] op_sel_hi:[1,0,0] neg_lo:[0,0,1] neg_hi:[0,0,1]
	v_pk_fma_f32 v[176:177], v[18:19], s[40:41], v[192:193] op_sel_hi:[1,0,0] neg_lo:[0,0,1] neg_hi:[0,0,1]
	v_cndmask_b32_e64 v88, v33, 1.0, vcc
	v_add3_u32 v211, s67, v16, v72
	s_add_i32 s17, s2, -2
	v_cmp_gt_u32_e64 s[2:3], 32, v64
	v_mov_b64_e32 v[30:31], v[14:15]
	v_mov_b64_e32 v[46:47], v[14:15]
	v_mov_b64_e32 v[78:79], v[14:15]
	v_mov_b32_e32 v117, v112
	v_mov_b32_e32 v118, v112
	v_mov_b32_e32 v119, v112
	v_lshlrev_b32_e32 v208, 2, v109
	v_mul_lo_u32 v215, v213, s65
	v_lshl_add_u32 v214, v109, 4, s79
	s_add_i32 s20, s74, -1
	v_lshl_add_u64 v[194:195], s[4:5], 0, v[190:191]
	v_lshl_add_u64 v[196:197], s[4:5], 0, v[188:189]
	v_lshl_add_u64 v[198:199], s[44:45], 0, v[104:105]
	s_mov_b32 s21, 0
	s_movk_i32 s22, 0x80
	v_mov_b64_e32 v[28:29], v[12:13]
	v_mov_b64_e32 v[26:27], v[10:11]
	v_mov_b64_e32 v[24:25], v[8:9]
	v_mov_b64_e32 v[22:23], v[6:7]
	v_mov_b64_e32 v[20:21], v[4:5]
	v_mov_b64_e32 v[18:19], v[2:3]
	v_mov_b64_e32 v[16:17], v[0:1]
	v_mov_b64_e32 v[44:45], v[12:13]
	v_mov_b64_e32 v[42:43], v[10:11]
	v_mov_b64_e32 v[40:41], v[8:9]
	v_mov_b64_e32 v[38:39], v[6:7]
	v_mov_b64_e32 v[36:37], v[4:5]
	v_mov_b64_e32 v[34:35], v[2:3]
	v_mov_b64_e32 v[32:33], v[0:1]
	v_mov_b64_e32 v[60:61], v[12:13]
	v_mov_b64_e32 v[58:59], v[10:11]
	v_mov_b64_e32 v[56:57], v[8:9]
	v_mov_b64_e32 v[54:55], v[6:7]
	v_mov_b64_e32 v[52:53], v[4:5]
	v_mov_b64_e32 v[50:51], v[2:3]
	v_mov_b64_e32 v[48:49], v[0:1]
	v_mov_b64_e32 v[76:77], v[12:13]
	v_mov_b64_e32 v[74:75], v[10:11]
	v_mov_b64_e32 v[72:73], v[8:9]
	v_mov_b64_e32 v[70:71], v[6:7]
	v_mov_b64_e32 v[68:69], v[4:5]
	v_mov_b64_e32 v[66:67], v[2:3]
	v_mov_b64_e32 v[64:65], v[0:1]
	s_branch .LBB0_566

.LBB0_584:
	s_waitcnt lgkmcnt(4)
	v_mfma_scale_f32_32x32x64_f8f6f4 v[80:95], v[80:87], v[120:127], 0, v205, v205 op_sel_hi:[0,0,0]
	s_lshr_b32 s17, s17, 1
	s_add_i32 s17, s17, 1
	s_mov_b64 s[4:5], exec
	s_cmp_ge_u32 s17, s74
	s_waitcnt lgkmcnt(2)
	v_mfma_scale_f32_32x32x64_f8f6f4 v[80:95], v[104:111], v[128:135], v[80:95], v205, v205 op_sel_hi:[0,0,0]
	s_waitcnt lgkmcnt(0)
	v_mfma_scale_f32_32x32x64_f8f6f4 v[80:95], v[96:103], v[136:143], v[80:95], v205, v205 op_sel_hi:[0,0,0]
	s_nop 15
	s_nop 3
	v_max_f32_e32 v96, v80, v81
	v_max3_f32 v96, v96, v82, v83
	v_max3_f32 v96, v96, v84, v85
	v_max3_f32 v96, v96, v86, v87
	v_max3_f32 v96, v96, v88, v89
	v_max3_f32 v96, v96, v90, v91
	v_max3_f32 v96, v96, v92, v93
	v_max3_f32 v96, v96, v94, v95
	v_mov_b32_e32 v97, v96
	s_nop 1
	v_permlane32_swap_b32_e32 v96, v97
	v_max_f32_e32 v96, v96, v97
	v_fma_f32 v97, v96, s40, -v192
	v_cmp_ge_f32_e32 vcc, s70, v97
	s_cbranch_scc1 .LBB0_588
	s_waitcnt vmcnt(1)
	ds_write_b128 v206, v[168:171]
	s_and_saveexec_b64 s[18:19], s[0:1]
	v_add3_u32 v97, 0, v215, v188
	ds_write_b128 v97, v[164:167]
	s_or_b64 exec, exec, s[18:19]
	s_waitcnt vmcnt(0)
	ds_write_b128 v207, v[172:175]
.LBB0_588:
	v_mul_f32_e32 v96, 0x3dd53b94, v96
	v_add_f32_e32 v96, 0xc0a00000, v96
	v_max_f32_e32 v124, v192, v96
	v_sub_f32_e32 v96, v192, v124
	v_exp_f32_e32 v96, v96
	v_exp_f32_e32 v97, v178
	v_exp_f32_e32 v98, v179
	s_cmp_eq_u64 vcc, s[4:5]
	v_exp_f32_e32 v99, v162
	v_exp_f32_e32 v102, v163
	s_cselect_b64 s[0:1], -1, 0
	v_exp_f32_e32 v105, v158
	v_exp_f32_e32 v106, v159
	v_exp_f32_e32 v109, v154
	v_exp_f32_e32 v110, v155
	v_cndmask_b32_e64 v125, v96, 1.0, s[0:1]
	v_mov_b32_e32 v96, v187
	v_cvt_pk_fp8_f32 v96, v97, v98
	v_mov_b32_e32 v97, v187
	v_cvt_pk_fp8_f32 v97, v99, v102
	v_mov_b32_e32 v98, v187
	v_mov_b32_e32 v99, v187
	v_exp_f32_e32 v100, v176
	v_exp_f32_e32 v101, v177
	v_exp_f32_e32 v103, v160
	v_exp_f32_e32 v104, v161
	v_exp_f32_e32 v107, v156
	v_exp_f32_e32 v108, v157
	v_exp_f32_e32 v111, v152
	v_exp_f32_e32 v120, v153
	v_cvt_pk_fp8_f32 v98, v105, v106
	v_cvt_pk_fp8_f32 v99, v109, v110
	v_cvt_pk_fp8_f32 v96, v100, v101 op_sel:[0,0,1]
	v_cvt_pk_fp8_f32 v97, v103, v104 op_sel:[0,0,1]
	v_cvt_pk_fp8_f32 v98, v107, v108 op_sel:[0,0,1]
	v_cvt_pk_fp8_f32 v99, v111, v120 op_sel:[0,0,1]
	v_cmp_gt_f32_e32 vcc, 1.0, v125
	s_waitcnt lgkmcnt(0)
	s_barrier
	s_cbranch_vccz .LBB0_592
	s_and_saveexec_b64 s[4:5], s[2:3]
	ds_write_b32 v209, v125 offset:128
	s_or_b64 exec, exec, s[4:5]
	v_cvt_f32_fp8_e32 v126, v96
	v_cvt_f32_fp8_sdwa v127, v96 src0_sel:BYTE_1
	v_cvt_f32_fp8_sdwa v128, v96 src0_sel:BYTE_2
	v_cvt_f32_fp8_sdwa v96, v96 src0_sel:BYTE_3
	v_mul_f32_e32 v126, v125, v126
	v_mul_f32_e32 v127, v125, v127
	v_med3_f32 v126, v126, s69, v203
	v_mul_f32_e32 v96, v125, v96
	v_med3_f32 v127, v127, s69, v203
	v_med3_f32 v129, v96, s69, v203
	v_mov_b32_e32 v96, v187
	v_cvt_pk_fp8_f32 v96, v126, v127
	v_cvt_f32_fp8_e32 v126, v97
	v_cvt_f32_fp8_sdwa v127, v97 src0_sel:BYTE_1
	v_mul_f32_e32 v128, v125, v128
	v_med3_f32 v128, v128, s69, v203
	v_cvt_f32_fp8_sdwa v130, v97 src0_sel:BYTE_2
	v_cvt_pk_fp8_f32 v96, v128, v129 op_sel:[0,0,1]
	v_mul_f32_e32 v126, v125, v126
	v_mul_f32_e32 v127, v125, v127
	v_cvt_f32_fp8_sdwa v129, v97 src0_sel:BYTE_3
	v_med3_f32 v126, v126, s69, v203
	v_med3_f32 v127, v127, s69, v203
	v_mov_b32_e32 v97, v187
	v_cvt_pk_fp8_f32 v97, v126, v127
	v_mul_f32_e32 v128, v125, v130
	v_mul_f32_e32 v126, v125, v129
	v_med3_f32 v127, v128, s69, v203
	v_med3_f32 v126, v126, s69, v203
	v_cvt_pk_fp8_f32 v97, v127, v126 op_sel:[0,0,1]
	v_cvt_f32_fp8_e32 v126, v98
	v_cvt_f32_fp8_sdwa v127, v98 src0_sel:BYTE_1
	v_cvt_f32_fp8_sdwa v128, v98 src0_sel:BYTE_2
	v_cvt_f32_fp8_sdwa v98, v98 src0_sel:BYTE_3
	v_mul_f32_e32 v126, v125, v126
	v_mul_f32_e32 v127, v125, v127
	v_med3_f32 v126, v126, s69, v203
	v_mul_f32_e32 v98, v125, v98
	v_med3_f32 v127, v127, s69, v203
	v_med3_f32 v129, v98, s69, v203
	v_mov_b32_e32 v98, v187
	v_cvt_pk_fp8_f32 v98, v126, v127
	v_cvt_f32_fp8_e32 v126, v99
	v_cvt_f32_fp8_sdwa v127, v99 src0_sel:BYTE_1
	v_mul_f32_e32 v128, v125, v128
	v_med3_f32 v128, v128, s69, v203
	v_cvt_f32_fp8_sdwa v130, v99 src0_sel:BYTE_2
	v_cvt_pk_fp8_f32 v98, v128, v129 op_sel:[0,0,1]
	v_mul_f32_e32 v126, v125, v126
	v_mul_f32_e32 v127, v125, v127
	v_cvt_f32_fp8_sdwa v129, v99 src0_sel:BYTE_3
	v_med3_f32 v126, v126, s69, v203
	v_med3_f32 v127, v127, s69, v203
	v_mov_b32_e32 v99, v187
	v_cvt_pk_fp8_f32 v99, v126, v127
	s_waitcnt lgkmcnt(0)
	ds_read_b128 v[120:123], v214 offset:224
	ds_read_b128 v[108:111], v214 offset:192
	ds_read_b128 v[104:107], v214 offset:160
	ds_read_b128 v[100:103], v214 offset:128
	v_mul_f32_e32 v128, v125, v130
	v_mul_f32_e32 v125, v125, v129
	v_med3_f32 v126, v128, s69, v203
	v_med3_f32 v125, v125, s69, v203
	v_cvt_pk_fp8_f32 v99, v126, v125 op_sel:[0,0,1]
	s_waitcnt lgkmcnt(3)
	v_pk_mul_f32 v[62:63], v[62:63], v[122:123]
	s_waitcnt lgkmcnt(2)
	v_pk_mul_f32 v[58:59], v[58:59], v[110:111]
	s_waitcnt lgkmcnt(1)
	v_pk_mul_f32 v[54:55], v[54:55], v[106:107]
	s_waitcnt lgkmcnt(0)
	v_pk_mul_f32 v[50:51], v[50:51], v[102:103]
	v_pk_mul_f32 v[60:61], v[60:61], v[120:121]
	v_pk_mul_f32 v[56:57], v[56:57], v[108:109]
	v_pk_mul_f32 v[52:53], v[52:53], v[104:105]
	v_pk_mul_f32 v[48:49], v[48:49], v[100:101]
	v_pk_mul_f32 v[46:47], v[46:47], v[122:123]
	v_pk_mul_f32 v[42:43], v[42:43], v[110:111]
	v_pk_mul_f32 v[38:39], v[38:39], v[106:107]
	v_pk_mul_f32 v[34:35], v[34:35], v[102:103]
	v_pk_mul_f32 v[44:45], v[44:45], v[120:121]
	v_pk_mul_f32 v[40:41], v[40:41], v[108:109]
	v_pk_mul_f32 v[36:37], v[36:37], v[104:105]
	v_pk_mul_f32 v[32:33], v[32:33], v[100:101]
	v_pk_mul_f32 v[30:31], v[30:31], v[122:123]
	v_pk_mul_f32 v[26:27], v[26:27], v[110:111]
	v_pk_mul_f32 v[22:23], v[22:23], v[106:107]
	v_pk_mul_f32 v[18:19], v[18:19], v[102:103]
	v_pk_mul_f32 v[28:29], v[28:29], v[120:121]
	v_pk_mul_f32 v[24:25], v[24:25], v[108:109]
	v_pk_mul_f32 v[20:21], v[20:21], v[104:105]
	v_pk_mul_f32 v[16:17], v[16:17], v[100:101]
	v_pk_mul_f32 v[14:15], v[14:15], v[122:123]
	v_pk_mul_f32 v[10:11], v[10:11], v[110:111]
	v_pk_mul_f32 v[6:7], v[6:7], v[106:107]
	v_pk_mul_f32 v[2:3], v[2:3], v[102:103]
	v_pk_mul_f32 v[12:13], v[12:13], v[120:121]
	v_pk_mul_f32 v[8:9], v[8:9], v[108:109]
	v_pk_mul_f32 v[4:5], v[4:5], v[104:105]
	v_pk_mul_f32 v[0:1], v[0:1], v[100:101]
	v_pk_mul_f32 v[78:79], v[78:79], v[122:123]
	v_pk_mul_f32 v[74:75], v[74:75], v[110:111]
	v_pk_mul_f32 v[70:71], v[70:71], v[106:107]
	v_pk_mul_f32 v[66:67], v[66:67], v[102:103]
	v_pk_mul_f32 v[76:77], v[76:77], v[120:121]
	v_pk_mul_f32 v[72:73], v[72:73], v[108:109]
	v_pk_mul_f32 v[68:69], v[68:69], v[104:105]
	v_pk_mul_f32 v[64:65], v[64:65], v[100:101]

.LBB0_623:
	s_nop 7
	v_max_f32_e32 v48, v32, v33
	v_max3_f32 v48, v48, v34, v35
	v_max3_f32 v48, v48, v36, v37
	v_max3_f32 v48, v48, v38, v39
	v_max3_f32 v48, v48, v40, v41
	v_max3_f32 v48, v48, v42, v43
	v_max3_f32 v48, v48, v44, v45
	v_max3_f32 v48, v48, v46, v47
	v_mov_b32_e32 v49, v48
	s_nop 1
	v_permlane32_swap_b32_e32 v48, v49
	v_max_f32_e32 v48, v48, v49
	v_sub_f32_e32 v49, v48, v130
	v_cmp_ge_f32_e32 vcc, s54, v49
	s_cmp_eq_u64 vcc, exec
	v_max_f32_e32 v48, v130, v48
	s_cselect_b64 vcc, -1, 0
	v_sub_f32_e32 v49, v130, v48
	v_cndmask_b32_e32 v130, v48, v130, vcc
	v_sub_f32_e32 v32, v32, v130
	v_exp_f32_e32 v32, v32
	v_sub_f32_e32 v33, v33, v130
	v_exp_f32_e32 v33, v33
	v_sub_f32_e32 v34, v34, v130
	v_exp_f32_e32 v34, v34
	v_sub_f32_e32 v35, v35, v130
	v_exp_f32_e32 v35, v35
	v_sub_f32_e32 v36, v36, v130
	v_exp_f32_e32 v36, v36
	v_sub_f32_e32 v37, v37, v130
	v_add_f32_e32 v48, 0, v32
	v_exp_f32_e32 v37, v37
	v_sub_f32_e32 v38, v38, v130
	v_add_f32_e32 v48, v33, v48
	v_exp_f32_e32 v38, v38
	v_sub_f32_e32 v39, v39, v130
	v_add_f32_e32 v48, v34, v48
	v_exp_f32_e32 v39, v39
	v_sub_f32_e32 v40, v40, v130
	v_add_f32_e32 v48, v35, v48
	v_exp_f32_e32 v40, v40
	v_sub_f32_e32 v41, v41, v130
	v_add_f32_e32 v48, v36, v48
	v_exp_f32_e32 v41, v41
	v_sub_f32_e32 v42, v42, v130
	v_add_f32_e32 v48, v37, v48
	v_exp_f32_e32 v42, v42
	v_sub_f32_e32 v43, v43, v130
	v_add_f32_e32 v48, v38, v48
	v_exp_f32_e32 v43, v43
	v_sub_f32_e32 v44, v44, v130
	v_add_f32_e32 v48, v39, v48
	v_exp_f32_e32 v44, v44
	v_sub_f32_e32 v45, v45, v130
	v_add_f32_e32 v48, v40, v48
	v_exp_f32_e32 v45, v45
	v_sub_f32_e32 v46, v46, v130
	v_add_f32_e32 v48, v41, v48
	v_exp_f32_e32 v46, v46
	v_sub_f32_e32 v47, v47, v130
	v_add_f32_e32 v48, v42, v48
	v_exp_f32_e32 v47, v47
	v_add_f32_e32 v48, v43, v48
	v_exp_f32_e32 v49, v49
	v_add_f32_e32 v48, v44, v48
	v_add_f32_e32 v48, v45, v48
	v_add_f32_e32 v48, v46, v48
	v_add_f32_e32 v132, v47, v48
	v_cndmask_b32_e64 v131, v49, 1.0, vcc
	v_mov_b32_e32 v133, v132
	v_cvt_pk_bf16_f32 v32, v32, v33
	v_cvt_pk_bf16_f32 v33, v34, v35
	v_cvt_pk_bf16_f32 v34, v36, v37
	v_cvt_pk_bf16_f32 v35, v38, v39
	v_cvt_pk_bf16_f32 v36, v40, v41
	v_cvt_pk_bf16_f32 v37, v42, v43
	v_cvt_pk_bf16_f32 v38, v44, v45
	v_cvt_pk_bf16_f32 v39, v46, v47
	s_nop 1
	v_permlane32_swap_b32_e32 v132, v133
	v_permlane32_swap_b32_e32 v32, v34
	v_permlane32_swap_b32_e32 v33, v35
	v_permlane32_swap_b32_e32 v36, v38
	v_permlane32_swap_b32_e32 v37, v39
	v_cmp_gt_f32_e32 vcc, 1.0, v131
	s_cbranch_vccz .LBB0_627
	s_and_saveexec_b64 s[22:23], s[0:1]
	ds_write_b32 v116, v131 offset:128
	s_or_b64 exec, exec, s[22:23]
	s_waitcnt lgkmcnt(0)
	ds_read_b128 v[40:43], v126 offset:224
	ds_read_b128 v[44:47], v126 offset:192
	ds_read_b128 v[48:51], v126 offset:160
	ds_read_b128 v[52:55], v126 offset:128
	s_waitcnt lgkmcnt(3)
	v_pk_mul_f32 v[14:15], v[14:15], v[42:43]
	s_waitcnt lgkmcnt(2)
	v_pk_mul_f32 v[10:11], v[10:11], v[46:47]
	s_waitcnt lgkmcnt(1)
	v_pk_mul_f32 v[6:7], v[6:7], v[50:51]
	s_waitcnt lgkmcnt(0)
	v_pk_mul_f32 v[2:3], v[2:3], v[54:55]
	v_pk_mul_f32 v[30:31], v[30:31], v[42:43]
	v_pk_mul_f32 v[26:27], v[26:27], v[46:47]
	v_pk_mul_f32 v[22:23], v[22:23], v[50:51]
	v_pk_mul_f32 v[18:19], v[18:19], v[54:55]
	v_pk_mul_f32 v[12:13], v[12:13], v[40:41]
	v_pk_mul_f32 v[8:9], v[8:9], v[44:45]
	v_pk_mul_f32 v[4:5], v[4:5], v[48:49]
	v_pk_mul_f32 v[0:1], v[0:1], v[52:53]
	v_pk_mul_f32 v[28:29], v[28:29], v[40:41]
	v_pk_mul_f32 v[24:25], v[24:25], v[44:45]
	v_pk_mul_f32 v[20:21], v[20:21], v[48:49]
	v_pk_mul_f32 v[16:17], v[16:17], v[52:53]

.LBB0_631:
	s_nop 8
	v_max_f32_e32 v48, v32, v33
	v_max3_f32 v48, v48, v34, v35
	v_max3_f32 v48, v48, v36, v37
	v_max3_f32 v48, v48, v38, v39
	v_max3_f32 v48, v48, v40, v41
	v_max3_f32 v48, v48, v42, v43
	v_max3_f32 v48, v48, v44, v45
	v_max3_f32 v48, v48, v46, v47
	v_mov_b32_e32 v49, v48
	s_nop 1
	v_permlane32_swap_b32_e32 v48, v49
	v_max_f32_e32 v48, v48, v49
	v_sub_f32_e32 v49, v48, v130
	v_cmp_ge_f32_e32 vcc, s54, v49
	s_cmp_eq_u64 vcc, exec
	v_max_f32_e32 v48, v130, v48
	s_cselect_b64 vcc, -1, 0
	v_sub_f32_e32 v49, v130, v48
	v_cndmask_b32_e32 v130, v48, v130, vcc
	v_sub_f32_e32 v40, v40, v130
	v_exp_f32_e32 v48, v40
	v_sub_f32_e32 v40, v41, v130
	v_exp_f32_e32 v50, v40
	v_sub_f32_e32 v40, v42, v130
	v_sub_f32_e32 v32, v32, v130
	v_exp_f32_e32 v51, v40
	v_sub_f32_e32 v40, v43, v130
	v_exp_f32_e32 v32, v32
	v_sub_f32_e32 v33, v33, v130
	v_exp_f32_e32 v43, v40
	v_sub_f32_e32 v40, v44, v130
	v_exp_f32_e32 v33, v33
	v_sub_f32_e32 v34, v34, v130
	v_exp_f32_e32 v44, v40
	v_sub_f32_e32 v40, v45, v130
	v_exp_f32_e32 v34, v34
	v_sub_f32_e32 v35, v35, v130
	v_exp_f32_e32 v45, v40
	v_sub_f32_e32 v40, v46, v130
	v_exp_f32_e32 v35, v35
	v_sub_f32_e32 v36, v36, v130
	v_exp_f32_e32 v46, v40
	v_sub_f32_e32 v40, v47, v130
	v_exp_f32_e32 v36, v36
	v_sub_f32_e32 v37, v37, v130
	v_exp_f32_e32 v47, v40
	v_add_f32_e32 v40, 0, v32
	v_exp_f32_e32 v37, v37
	v_sub_f32_e32 v38, v38, v130
	v_add_f32_e32 v40, v33, v40
	v_exp_f32_e32 v38, v38
	v_sub_f32_e32 v39, v39, v130
	v_add_f32_e32 v40, v34, v40
	v_exp_f32_e32 v39, v39
	v_add_f32_e32 v40, v35, v40
	v_add_f32_e32 v40, v36, v40
	v_add_f32_e32 v40, v37, v40
	v_add_f32_e32 v40, v38, v40
	v_add_f32_e32 v40, v39, v40
	v_add_f32_e32 v40, v48, v40
	v_add_f32_e32 v40, v50, v40
	v_add_f32_e32 v40, v51, v40
	v_add_f32_e32 v40, v43, v40
	v_exp_f32_e32 v49, v49
	v_add_f32_e32 v40, v44, v40
	v_add_f32_e32 v40, v45, v40
	v_add_f32_e32 v40, v46, v40
	v_add_f32_e32 v41, v47, v40
	v_cndmask_b32_e64 v40, v49, 1.0, vcc
	v_mov_b32_e32 v42, v41
	v_cvt_pk_bf16_f32 v32, v32, v33
	v_cvt_pk_bf16_f32 v33, v34, v35
	v_cvt_pk_bf16_f32 v34, v36, v37
	v_cvt_pk_bf16_f32 v35, v38, v39
	v_cvt_pk_bf16_f32 v36, v48, v50
	v_cvt_pk_bf16_f32 v37, v51, v43
	v_cvt_pk_bf16_f32 v38, v44, v45
	v_cvt_pk_bf16_f32 v39, v46, v47
	s_nop 1
	v_permlane32_swap_b32_e32 v41, v42
	v_permlane32_swap_b32_e32 v32, v34
	v_permlane32_swap_b32_e32 v33, v35
	v_permlane32_swap_b32_e32 v36, v38
	v_permlane32_swap_b32_e32 v37, v39
	v_cmp_gt_f32_e32 vcc, 1.0, v40
	s_cbranch_vccz .LBB0_635
	s_and_saveexec_b64 s[2:3], s[0:1]
	ds_write_b32 v116, v40 offset:128
	s_or_b64 exec, exec, s[2:3]
	s_waitcnt lgkmcnt(0)
	ds_read_b128 v[44:47], v126 offset:224
	ds_read_b128 v[48:51], v126 offset:192
	ds_read_b128 v[52:55], v126 offset:160
	ds_read_b128 v[56:59], v126 offset:128
	s_waitcnt lgkmcnt(3)
	v_pk_mul_f32 v[30:31], v[30:31], v[46:47]
	s_waitcnt lgkmcnt(2)
	v_pk_mul_f32 v[26:27], v[26:27], v[50:51]
	s_waitcnt lgkmcnt(1)
	v_pk_mul_f32 v[22:23], v[22:23], v[54:55]
	s_waitcnt lgkmcnt(0)
	v_pk_mul_f32 v[18:19], v[18:19], v[58:59]
	v_pk_mul_f32 v[28:29], v[28:29], v[44:45]
	v_pk_mul_f32 v[24:25], v[24:25], v[48:49]
	v_pk_mul_f32 v[20:21], v[20:21], v[52:53]
	v_pk_mul_f32 v[16:17], v[16:17], v[56:57]
	v_pk_mul_f32 v[14:15], v[14:15], v[46:47]
	v_pk_mul_f32 v[10:11], v[10:11], v[50:51]
	v_pk_mul_f32 v[6:7], v[6:7], v[54:55]
	v_pk_mul_f32 v[2:3], v[2:3], v[58:59]
	v_pk_mul_f32 v[12:13], v[12:13], v[44:45]
	v_pk_mul_f32 v[8:9], v[8:9], v[48:49]
	v_pk_mul_f32 v[4:5], v[4:5], v[52:53]
	v_pk_mul_f32 v[0:1], v[0:1], v[56:57]

.LBB0_793:
	s_nop 8
	v_max_f32_e32 v82, v66, v67
	v_max3_f32 v82, v82, v68, v69
	v_max3_f32 v82, v82, v70, v71
	v_max3_f32 v82, v82, v72, v73
	v_max3_f32 v82, v82, v74, v75
	v_max3_f32 v82, v82, v76, v77
	v_max3_f32 v82, v82, v78, v79
	v_max3_f32 v82, v82, v80, v81
	v_mov_b32_e32 v83, v82
	s_nop 1
	v_permlane32_swap_b32_e32 v82, v83
	v_max_f32_e32 v82, v82, v83
	v_sub_f32_e32 v83, v82, v244
	v_cmp_ge_f32_e32 vcc, s63, v83
	s_cmp_eq_u64 vcc, exec
	v_max_f32_e32 v82, v244, v82
	s_cselect_b64 vcc, -1, 0
	v_sub_f32_e32 v83, v244, v82
	v_cndmask_b32_e32 v244, v82, v244, vcc
	v_sub_f32_e32 v66, v66, v244
	v_exp_f32_e32 v66, v66
	v_sub_f32_e32 v67, v67, v244
	v_exp_f32_e32 v67, v67
	v_sub_f32_e32 v68, v68, v244
	v_exp_f32_e32 v68, v68
	v_sub_f32_e32 v69, v69, v244
	v_exp_f32_e32 v69, v69
	v_sub_f32_e32 v70, v70, v244
	v_exp_f32_e32 v70, v70
	v_sub_f32_e32 v71, v71, v244
	v_add_f32_e32 v82, 0, v66
	v_exp_f32_e32 v71, v71
	v_sub_f32_e32 v72, v72, v244
	v_add_f32_e32 v82, v67, v82
	v_exp_f32_e32 v72, v72
	v_sub_f32_e32 v73, v73, v244
	v_add_f32_e32 v82, v68, v82
	v_exp_f32_e32 v73, v73
	v_sub_f32_e32 v74, v74, v244
	v_add_f32_e32 v82, v69, v82
	v_exp_f32_e32 v74, v74
	v_sub_f32_e32 v75, v75, v244
	v_add_f32_e32 v82, v70, v82
	v_exp_f32_e32 v75, v75
	v_sub_f32_e32 v76, v76, v244
	v_add_f32_e32 v82, v71, v82
	v_exp_f32_e32 v76, v76
	v_sub_f32_e32 v77, v77, v244
	v_add_f32_e32 v82, v72, v82
	v_exp_f32_e32 v77, v77
	v_sub_f32_e32 v78, v78, v244
	v_add_f32_e32 v82, v73, v82
	v_exp_f32_e32 v78, v78
	v_sub_f32_e32 v79, v79, v244
	v_add_f32_e32 v82, v74, v82
	v_exp_f32_e32 v79, v79
	v_sub_f32_e32 v80, v80, v244
	v_add_f32_e32 v82, v75, v82
	v_exp_f32_e32 v80, v80
	v_sub_f32_e32 v81, v81, v244
	v_add_f32_e32 v82, v76, v82
	v_exp_f32_e32 v81, v81
	v_add_f32_e32 v82, v77, v82
	v_exp_f32_e32 v83, v83
	v_add_f32_e32 v82, v78, v82
	v_add_f32_e32 v82, v79, v82
	v_add_f32_e32 v82, v80, v82
	v_add_f32_e32 v242, v81, v82
	v_cndmask_b32_e64 v241, v83, 1.0, vcc
	v_mov_b32_e32 v243, v242
	v_cvt_pk_bf16_f32 v66, v66, v67
	v_cvt_pk_bf16_f32 v67, v68, v69
	v_cvt_pk_bf16_f32 v68, v70, v71
	v_cvt_pk_bf16_f32 v69, v72, v73
	v_cvt_pk_bf16_f32 v70, v74, v75
	v_cvt_pk_bf16_f32 v71, v76, v77
	v_cvt_pk_bf16_f32 v72, v78, v79
	v_cvt_pk_bf16_f32 v73, v80, v81
	s_nop 1
	v_permlane32_swap_b32_e32 v242, v243
	v_permlane32_swap_b32_e32 v66, v68
	v_permlane32_swap_b32_e32 v67, v69
	v_permlane32_swap_b32_e32 v70, v72
	v_permlane32_swap_b32_e32 v71, v73
	v_cmp_gt_f32_e32 vcc, 1.0, v241
	s_cbranch_vccz .LBB0_797
	s_and_saveexec_b64 s[16:17], s[10:11]
	ds_write_b32 v192, v241 offset:128
	s_or_b64 exec, exec, s[16:17]
	s_waitcnt lgkmcnt(0)
	ds_read_b128 v[74:77], v218 offset:224
	ds_read_b128 v[78:81], v218 offset:192
	ds_read_b128 v[82:85], v218 offset:160
	ds_read_b128 v[86:89], v218 offset:128
	s_waitcnt lgkmcnt(3)
	v_pk_mul_f32 v[62:63], v[62:63], v[76:77]
	s_waitcnt lgkmcnt(2)
	v_pk_mul_f32 v[58:59], v[58:59], v[80:81]
	s_waitcnt lgkmcnt(1)
	v_pk_mul_f32 v[54:55], v[54:55], v[84:85]
	s_waitcnt lgkmcnt(0)
	v_pk_mul_f32 v[50:51], v[50:51], v[88:89]
	v_pk_mul_f32 v[60:61], v[60:61], v[74:75]
	v_pk_mul_f32 v[56:57], v[56:57], v[78:79]
	v_pk_mul_f32 v[52:53], v[52:53], v[82:83]
	v_pk_mul_f32 v[48:49], v[48:49], v[86:87]
	v_pk_mul_f32 v[46:47], v[46:47], v[76:77]
	v_pk_mul_f32 v[42:43], v[42:43], v[80:81]
	v_pk_mul_f32 v[38:39], v[38:39], v[84:85]
	v_pk_mul_f32 v[34:35], v[34:35], v[88:89]
	v_pk_mul_f32 v[44:45], v[44:45], v[74:75]
	v_pk_mul_f32 v[40:41], v[40:41], v[78:79]
	v_pk_mul_f32 v[36:37], v[36:37], v[82:83]
	v_pk_mul_f32 v[32:33], v[32:33], v[86:87]
	v_pk_mul_f32 v[30:31], v[30:31], v[76:77]
	v_pk_mul_f32 v[26:27], v[26:27], v[80:81]
	v_pk_mul_f32 v[22:23], v[22:23], v[84:85]
	v_pk_mul_f32 v[18:19], v[18:19], v[88:89]
	v_pk_mul_f32 v[28:29], v[28:29], v[74:75]
	v_pk_mul_f32 v[24:25], v[24:25], v[78:79]
	v_pk_mul_f32 v[20:21], v[20:21], v[82:83]
	v_pk_mul_f32 v[16:17], v[16:17], v[86:87]
	v_pk_mul_f32 v[14:15], v[14:15], v[76:77]
	v_pk_mul_f32 v[10:11], v[10:11], v[80:81]
	v_pk_mul_f32 v[6:7], v[6:7], v[84:85]
	v_pk_mul_f32 v[2:3], v[2:3], v[88:89]
	v_pk_mul_f32 v[12:13], v[12:13], v[74:75]
	v_pk_mul_f32 v[8:9], v[8:9], v[78:79]
	v_pk_mul_f32 v[4:5], v[4:5], v[82:83]
	v_pk_mul_f32 v[0:1], v[0:1], v[86:87]

.LBB0_833:
	s_nop 8
	v_max_f32_e32 v82, v66, v67
	v_max3_f32 v82, v82, v68, v69
	v_max3_f32 v82, v82, v70, v71
	v_max3_f32 v82, v82, v72, v73
	v_max3_f32 v82, v82, v74, v75
	v_max3_f32 v82, v82, v76, v77
	v_max3_f32 v82, v82, v78, v79
	v_max3_f32 v82, v82, v80, v81
	v_mov_b32_e32 v83, v82
	s_nop 1
	v_permlane32_swap_b32_e32 v82, v83
	v_max_f32_e32 v82, v82, v83
	v_sub_f32_e32 v83, v82, v244
	v_cmp_ge_f32_e32 vcc, s63, v83
	s_cmp_eq_u64 vcc, exec
	v_max_f32_e32 v82, v244, v82
	s_cselect_b64 vcc, -1, 0
	v_sub_f32_e32 v83, v244, v82
	v_cndmask_b32_e32 v244, v82, v244, vcc
	v_sub_f32_e32 v74, v74, v244
	v_exp_f32_e32 v82, v74
	v_sub_f32_e32 v74, v75, v244
	v_exp_f32_e32 v84, v74
	v_sub_f32_e32 v74, v76, v244
	v_sub_f32_e32 v66, v66, v244
	v_exp_f32_e32 v85, v74
	v_sub_f32_e32 v74, v77, v244
	v_exp_f32_e32 v66, v66
	v_sub_f32_e32 v67, v67, v244
	v_exp_f32_e32 v77, v74
	v_sub_f32_e32 v74, v78, v244
	v_exp_f32_e32 v67, v67
	v_sub_f32_e32 v68, v68, v244
	v_exp_f32_e32 v78, v74
	v_sub_f32_e32 v74, v79, v244
	v_exp_f32_e32 v68, v68
	v_sub_f32_e32 v69, v69, v244
	v_exp_f32_e32 v79, v74
	v_sub_f32_e32 v74, v80, v244
	v_exp_f32_e32 v69, v69
	v_sub_f32_e32 v70, v70, v244
	v_exp_f32_e32 v80, v74
	v_sub_f32_e32 v74, v81, v244
	v_exp_f32_e32 v70, v70
	v_sub_f32_e32 v71, v71, v244
	v_exp_f32_e32 v81, v74
	v_add_f32_e32 v74, 0, v66
	v_exp_f32_e32 v71, v71
	v_sub_f32_e32 v72, v72, v244
	v_add_f32_e32 v74, v67, v74
	v_exp_f32_e32 v72, v72
	v_sub_f32_e32 v73, v73, v244
	v_add_f32_e32 v74, v68, v74
	v_exp_f32_e32 v73, v73
	v_add_f32_e32 v74, v69, v74
	v_add_f32_e32 v74, v70, v74
	v_add_f32_e32 v74, v71, v74
	v_add_f32_e32 v74, v72, v74
	v_add_f32_e32 v74, v73, v74
	v_add_f32_e32 v74, v82, v74
	v_add_f32_e32 v74, v84, v74
	v_add_f32_e32 v74, v85, v74
	v_add_f32_e32 v74, v77, v74
	v_exp_f32_e32 v83, v83
	v_add_f32_e32 v74, v78, v74
	v_add_f32_e32 v74, v79, v74
	v_add_f32_e32 v74, v80, v74
	v_add_f32_e32 v75, v81, v74
	v_cndmask_b32_e64 v74, v83, 1.0, vcc
	v_mov_b32_e32 v76, v75
	v_cvt_pk_bf16_f32 v66, v66, v67
	v_cvt_pk_bf16_f32 v67, v68, v69
	v_cvt_pk_bf16_f32 v68, v70, v71
	v_cvt_pk_bf16_f32 v69, v72, v73
	v_cvt_pk_bf16_f32 v70, v82, v84
	v_cvt_pk_bf16_f32 v71, v85, v77
	v_cvt_pk_bf16_f32 v72, v78, v79
	v_cvt_pk_bf16_f32 v73, v80, v81
	s_nop 1
	v_permlane32_swap_b32_e32 v75, v76
	v_permlane32_swap_b32_e32 v66, v68
	v_permlane32_swap_b32_e32 v67, v69
	v_permlane32_swap_b32_e32 v70, v72
	v_permlane32_swap_b32_e32 v71, v73
	v_cmp_gt_f32_e32 vcc, 1.0, v74
	s_cbranch_vccz .LBB0_837
	s_and_saveexec_b64 s[12:13], s[10:11]
	ds_write_b32 v192, v74 offset:128
	s_or_b64 exec, exec, s[12:13]
	s_waitcnt lgkmcnt(0)
	ds_read_b128 v[78:81], v218 offset:224
	ds_read_b128 v[82:85], v218 offset:192
	ds_read_b128 v[86:89], v218 offset:160
	ds_read_b128 v[90:93], v218 offset:128
	s_waitcnt lgkmcnt(3)
	v_pk_mul_f32 v[62:63], v[62:63], v[80:81]
	s_waitcnt lgkmcnt(2)
	v_pk_mul_f32 v[58:59], v[58:59], v[84:85]
	s_waitcnt lgkmcnt(1)
	v_pk_mul_f32 v[54:55], v[54:55], v[88:89]
	s_waitcnt lgkmcnt(0)
	v_pk_mul_f32 v[50:51], v[50:51], v[92:93]
	v_pk_mul_f32 v[60:61], v[60:61], v[78:79]
	v_pk_mul_f32 v[56:57], v[56:57], v[82:83]
	v_pk_mul_f32 v[52:53], v[52:53], v[86:87]
	v_pk_mul_f32 v[48:49], v[48:49], v[90:91]
	v_pk_mul_f32 v[46:47], v[46:47], v[80:81]
	v_pk_mul_f32 v[42:43], v[42:43], v[84:85]
	v_pk_mul_f32 v[38:39], v[38:39], v[88:89]
	v_pk_mul_f32 v[34:35], v[34:35], v[92:93]
	v_pk_mul_f32 v[44:45], v[44:45], v[78:79]
	v_pk_mul_f32 v[40:41], v[40:41], v[82:83]
	v_pk_mul_f32 v[36:37], v[36:37], v[86:87]
	v_pk_mul_f32 v[32:33], v[32:33], v[90:91]
	v_pk_mul_f32 v[30:31], v[30:31], v[80:81]
	v_pk_mul_f32 v[26:27], v[26:27], v[84:85]
	v_pk_mul_f32 v[22:23], v[22:23], v[88:89]
	v_pk_mul_f32 v[18:19], v[18:19], v[92:93]
	v_pk_mul_f32 v[28:29], v[28:29], v[78:79]
	v_pk_mul_f32 v[24:25], v[24:25], v[82:83]
	v_pk_mul_f32 v[20:21], v[20:21], v[86:87]
	v_pk_mul_f32 v[16:17], v[16:17], v[90:91]
	v_pk_mul_f32 v[14:15], v[14:15], v[80:81]
	v_pk_mul_f32 v[10:11], v[10:11], v[84:85]
	v_pk_mul_f32 v[6:7], v[6:7], v[88:89]
	v_pk_mul_f32 v[2:3], v[2:3], v[92:93]
	v_pk_mul_f32 v[12:13], v[12:13], v[78:79]
	v_pk_mul_f32 v[8:9], v[8:9], v[82:83]
	v_pk_mul_f32 v[4:5], v[4:5], v[86:87]
	v_pk_mul_f32 v[0:1], v[0:1], v[90:91]

.LBB0_1873:
	s_or_b64 exec, exec, s[2:3]
	v_mul_f32_e32 v0, v106, v0
	v_mul_f32_e32 v1, v106, v1
	v_mul_f32_e32 v26, v106, v26
	v_mul_f32_e32 v0, v0, v113
	v_mul_f32_e32 v1, v1, v112
	v_mul_f32_e32 v26, v26, v135
	v_med3_f32 v0, v0, s67, v205
	v_med3_f32 v1, v1, s67, v205
	v_mov_b32_e32 v135, v187
	v_cvt_pk_fp8_f32 v135, v0, v1
	v_mul_f32_e32 v2, v106, v2
	v_mul_f32_e32 v3, v106, v3
	v_mul_f32_e32 v2, v2, v111
	v_mul_f32_e32 v3, v3, v110
	v_med3_f32 v0, v2, s67, v205
	v_med3_f32 v1, v3, s67, v205
	v_mul_f32_e32 v25, v106, v25
	v_cvt_pk_fp8_f32 v135, v0, v1 op_sel:[0,0,1]
	v_max_f32_e32 v0, v104, v104
	v_max_f32_e32 v1, v105, v105
	v_mul_f32_e32 v25, v25, v136
	v_med3_f32 v0, v0, s67, v205
	v_med3_f32 v1, v1, s67, v205
	v_mov_b32_e32 v136, v187
	v_cvt_pk_fp8_f32 v136, v0, v1
	v_max_f32_e32 v2, v100, v100
	v_max_f32_e32 v1, v101, v101
	v_med3_f32 v0, v2, s67, v205
	v_med3_f32 v1, v1, s67, v205
	v_mul_f32_e32 v24, v106, v24
	v_cvt_pk_fp8_f32 v136, v0, v1 op_sel:[0,0,1]
	v_max_f32_e32 v0, v98, v98
	v_max_f32_e32 v1, v99, v99
	v_mul_f32_e32 v24, v24, v137
	v_med3_f32 v0, v0, s67, v205
	v_med3_f32 v1, v1, s67, v205
	v_mov_b32_e32 v137, v187
	v_cvt_pk_fp8_f32 v137, v0, v1
	v_max_f32_e32 v2, v96, v96
	v_max_f32_e32 v1, v97, v97
	v_med3_f32 v0, v2, s67, v205
	v_med3_f32 v1, v1, s67, v205
	v_mul_f32_e32 v31, v106, v31
	v_cvt_pk_fp8_f32 v137, v0, v1 op_sel:[0,0,1]
	v_max_f32_e32 v0, v94, v94
	v_max_f32_e32 v1, v95, v95
	v_mul_f32_e32 v31, v31, v138
	v_med3_f32 v0, v0, s67, v205
	v_med3_f32 v1, v1, s67, v205
	v_mov_b32_e32 v138, v187
	v_cvt_pk_fp8_f32 v138, v0, v1
	v_max_f32_e32 v2, v92, v92
	v_max_f32_e32 v1, v93, v93
	v_med3_f32 v0, v2, s67, v205
	v_med3_f32 v1, v1, s67, v205
	v_mul_f32_e32 v30, v106, v30
	v_cvt_pk_fp8_f32 v138, v0, v1 op_sel:[0,0,1]
	v_max_f32_e32 v0, v90, v90
	v_max_f32_e32 v1, v91, v91
	v_mul_f32_e32 v30, v30, v139
	v_med3_f32 v0, v0, s67, v205
	v_med3_f32 v1, v1, s67, v205
	v_mov_b32_e32 v139, v187
	v_cvt_pk_fp8_f32 v139, v0, v1
	v_max_f32_e32 v2, v88, v88
	v_max_f32_e32 v1, v89, v89
	v_med3_f32 v0, v2, s67, v205
	v_med3_f32 v1, v1, s67, v205
	v_mul_f32_e32 v29, v106, v29
	v_cvt_pk_fp8_f32 v139, v0, v1 op_sel:[0,0,1]
	v_max_f32_e32 v0, v86, v86
	v_max_f32_e32 v1, v87, v87
	v_mul_f32_e32 v29, v29, v140
	v_med3_f32 v0, v0, s67, v205
	v_med3_f32 v1, v1, s67, v205
	v_mov_b32_e32 v140, v187
	v_cvt_pk_fp8_f32 v140, v0, v1
	v_max_f32_e32 v2, v84, v84
	v_max_f32_e32 v1, v85, v85
	v_med3_f32 v0, v2, s67, v205
	v_med3_f32 v1, v1, s67, v205
	v_mul_f32_e32 v28, v106, v28
	v_cvt_pk_fp8_f32 v140, v0, v1 op_sel:[0,0,1]
	v_max_f32_e32 v0, v82, v82
	v_max_f32_e32 v1, v83, v83
	v_mul_f32_e32 v28, v28, v141
	v_med3_f32 v0, v0, s67, v205
	v_med3_f32 v1, v1, s67, v205
	v_mov_b32_e32 v141, v187
	v_cvt_pk_fp8_f32 v141, v0, v1
	v_max_f32_e32 v2, v80, v80
	v_max_f32_e32 v1, v81, v81
	v_med3_f32 v0, v2, s67, v205
	v_med3_f32 v1, v1, s67, v205
	v_mul_f32_e32 v35, v106, v35
	v_cvt_pk_fp8_f32 v141, v0, v1 op_sel:[0,0,1]
	v_max_f32_e32 v0, v78, v78
	v_max_f32_e32 v1, v79, v79
	v_mul_f32_e32 v35, v35, v142
	v_med3_f32 v0, v0, s67, v205
	v_med3_f32 v1, v1, s67, v205
	v_mov_b32_e32 v142, v187
	v_cvt_pk_fp8_f32 v142, v0, v1
	v_mul_f32_e32 v8, v106, v8
	v_mul_f32_e32 v9, v106, v9
	v_mul_f32_e32 v4, v106, v4
	v_mul_f32_e32 v5, v106, v5
	v_mul_f32_e32 v60, v60, v106
	v_mul_f32_e32 v61, v61, v106
	v_mul_f32_e32 v56, v56, v106
	v_mul_f32_e32 v57, v57, v106
	v_mul_f32_e32 v52, v52, v106
	v_mul_f32_e32 v53, v106, v53
	v_mul_f32_e32 v48, v106, v48
	v_mul_f32_e32 v49, v106, v49
	v_mul_f32_e32 v44, v106, v44
	v_mul_f32_e32 v45, v106, v45
	v_mul_f32_e32 v40, v106, v40
	v_mul_f32_e32 v41, v106, v41
	v_mul_f32_e32 v36, v106, v36
	v_mul_f32_e32 v37, v106, v37
	v_mul_f32_e32 v32, v106, v32
	v_mul_f32_e32 v33, v106, v33
	v_mul_f32_e32 v27, v106, v27
	v_mul_f32_e32 v20, v106, v20
	v_mul_f32_e32 v8, v8, v121
	v_mul_f32_e32 v9, v9, v120
	v_mul_f32_e32 v4, v4, v117
	v_mul_f32_e32 v5, v5, v116
	v_max_f32_e32 v2, v76, v76
	v_max_f32_e32 v1, v77, v77
	v_mul_f32_e32 v60, v60, v181
	v_mul_f32_e32 v61, v61, v180
	v_mul_f32_e32 v56, v56, v177
	v_mul_f32_e32 v57, v57, v176
	v_mul_f32_e32 v52, v52, v173
	v_mul_f32_e32 v53, v53, v172
	v_mul_f32_e32 v48, v48, v161
	v_mul_f32_e32 v49, v49, v160
	v_mul_f32_e32 v44, v44, v157
	v_mul_f32_e32 v45, v45, v156
	v_mul_f32_e32 v40, v40, v153
	v_mul_f32_e32 v41, v41, v152
	v_mul_f32_e32 v36, v36, v149
	v_mul_f32_e32 v37, v37, v148
	v_mul_f32_e32 v32, v32, v145
	v_mul_f32_e32 v33, v33, v144
	v_mul_f32_e32 v27, v27, v134
	v_mul_f32_e32 v20, v20, v133
	v_mul_f32_e32 v18, v106, v18
	v_mul_f32_e32 v19, v106, v19
	v_mul_f32_e32 v12, v106, v12
	v_mul_f32_e32 v13, v106, v13
	v_mul_f32_e32 v14, v106, v14
	v_mul_f32_e32 v15, v106, v15
	v_med3_f32 v8, v8, s67, v205
	v_med3_f32 v9, v9, s67, v205
	v_mov_b32_e32 v133, v187
	v_med3_f32 v4, v4, s67, v205
	v_med3_f32 v5, v5, s67, v205
	v_mov_b32_e32 v134, v187
	v_med3_f32 v0, v2, s67, v205
	v_med3_f32 v1, v1, s67, v205
	v_mul_f32_e32 v34, v106, v34
	v_mul_f32_e32 v18, v18, v127
	v_mul_f32_e32 v19, v19, v126
	v_mul_f32_e32 v12, v12, v125
	v_mul_f32_e32 v13, v13, v124
	v_mul_f32_e32 v14, v14, v123
	v_mul_f32_e32 v15, v15, v122
	v_med3_f32 v60, v60, s67, v205
	v_med3_f32 v61, v61, s67, v205
	v_mov_b32_e32 v120, v187
	v_med3_f32 v56, v56, s67, v205
	v_med3_f32 v57, v57, s67, v205
	v_mov_b32_e32 v121, v187
	v_med3_f32 v52, v52, s67, v205
	v_med3_f32 v53, v53, s67, v205
	v_mov_b32_e32 v122, v187
	v_med3_f32 v48, v48, s67, v205
	v_med3_f32 v49, v49, s67, v205
	v_mov_b32_e32 v123, v187
	v_med3_f32 v44, v44, s67, v205
	v_med3_f32 v45, v45, s67, v205
	v_mov_b32_e32 v124, v187
	v_med3_f32 v40, v40, s67, v205
	v_med3_f32 v41, v41, s67, v205
	v_mov_b32_e32 v125, v187
	v_med3_f32 v36, v36, s67, v205
	v_med3_f32 v37, v37, s67, v205
	v_mov_b32_e32 v126, v187
	v_med3_f32 v32, v32, s67, v205
	v_med3_f32 v33, v33, s67, v205
	v_mov_b32_e32 v127, v187
	v_cvt_pk_fp8_f32 v133, v8, v9
	v_cvt_pk_fp8_f32 v134, v4, v5
	v_cvt_pk_fp8_f32 v142, v0, v1 op_sel:[0,0,1]
	v_max_f32_e32 v0, v74, v74
	v_max_f32_e32 v1, v75, v75
	s_and_b32 s2, s18, 0x3fffffc0
	v_mul_f32_e32 v34, v34, v143
	v_mul_f32_e32 v10, v106, v10
	v_mul_f32_e32 v11, v106, v11
	v_mul_f32_e32 v6, v106, v6
	v_mul_f32_e32 v7, v106, v7
	v_cvt_pk_fp8_f32 v120, v60, v61
	v_cvt_pk_fp8_f32 v121, v56, v57
	v_cvt_pk_fp8_f32 v122, v52, v53
	v_cvt_pk_fp8_f32 v123, v48, v49
	v_cvt_pk_fp8_f32 v124, v44, v45
	v_cvt_pk_fp8_f32 v125, v40, v41
	v_cvt_pk_fp8_f32 v126, v36, v37
	v_cvt_pk_fp8_f32 v127, v32, v33
	v_med3_f32 v0, v0, s67, v205
	v_med3_f32 v1, v1, s67, v205
	v_mov_b32_e32 v143, v187
	s_lshl_b32 s2, s2, 2
	v_mul_f32_e32 v62, v62, v106
	v_mul_f32_e32 v63, v63, v106
	v_mul_f32_e32 v58, v58, v106
	v_mul_f32_e32 v59, v59, v106
	v_mul_f32_e32 v54, v106, v54
	v_mul_f32_e32 v55, v106, v55
	v_mul_f32_e32 v50, v106, v50
	v_mul_f32_e32 v51, v106, v51
	v_mul_f32_e32 v46, v106, v46
	v_mul_f32_e32 v47, v106, v47
	v_mul_f32_e32 v42, v106, v42
	v_mul_f32_e32 v43, v106, v43
	v_mul_f32_e32 v38, v106, v38
	v_mul_f32_e32 v39, v106, v39
	v_mul_f32_e32 v21, v106, v21
	v_mul_f32_e32 v16, v106, v16
	v_mul_f32_e32 v17, v106, v17
	v_mul_f32_e32 v10, v10, v119
	v_mul_f32_e32 v11, v11, v118
	v_mul_f32_e32 v6, v6, v115
	v_mul_f32_e32 v7, v7, v114
	v_cvt_pk_fp8_f32 v143, v0, v1
	v_mul_u32_u24_e32 v0, 0xd0, v188
	s_add_i32 s2, s2, 0
	v_mul_f32_e32 v62, v62, v179
	v_mul_f32_e32 v63, v63, v178
	v_mul_f32_e32 v58, v58, v175
	v_mul_f32_e32 v59, v59, v174
	v_mul_f32_e32 v54, v54, v163
	v_mul_f32_e32 v55, v55, v162
	v_mul_f32_e32 v50, v50, v159
	v_mul_f32_e32 v51, v51, v158
	v_mul_f32_e32 v46, v46, v155
	v_mul_f32_e32 v47, v47, v154
	v_mul_f32_e32 v42, v42, v151
	v_mul_f32_e32 v43, v43, v150
	v_mul_f32_e32 v38, v38, v147
	v_mul_f32_e32 v39, v39, v146
	v_mul_f32_e32 v21, v21, v132
	v_mul_f32_e32 v22, v106, v22
	v_mul_f32_e32 v23, v106, v23
	v_mul_f32_e32 v16, v16, v129
	v_mul_f32_e32 v17, v17, v128
	v_med3_f32 v8, v10, s67, v205
	v_med3_f32 v9, v11, s67, v205
	v_med3_f32 v6, v6, s67, v205
	v_med3_f32 v7, v7, s67, v205
	v_max_f32_e32 v2, v72, v72
	v_add3_u32 v214, 0, v0, v186
	s_add_i32 s77, s2, 0x18000
	s_ashr_i32 s2, s19, 6
	v_mul_f32_e32 v22, v22, v131
	v_mul_f32_e32 v23, v23, v130
	v_med3_f32 v62, v62, s67, v205
	v_med3_f32 v63, v63, s67, v205
	v_med3_f32 v56, v58, s67, v205
	v_med3_f32 v57, v59, s67, v205
	v_med3_f32 v54, v54, s67, v205
	v_med3_f32 v55, v55, s67, v205
	v_med3_f32 v48, v50, s67, v205
	v_med3_f32 v49, v51, s67, v205
	v_med3_f32 v46, v46, s67, v205
	v_med3_f32 v47, v47, s67, v205
	v_med3_f32 v40, v42, s67, v205
	v_med3_f32 v41, v43, s67, v205
	v_med3_f32 v38, v38, s67, v205
	v_med3_f32 v39, v39, s67, v205
	v_med3_f32 v32, v34, s67, v205
	v_med3_f32 v33, v35, s67, v205
	v_med3_f32 v28, v28, s67, v205
	v_med3_f32 v29, v29, s67, v205
	v_mov_b32_e32 v128, v187
	v_med3_f32 v24, v24, s67, v205
	v_med3_f32 v25, v25, s67, v205
	v_mov_b32_e32 v129, v187
	v_med3_f32 v20, v20, s67, v205
	v_med3_f32 v21, v21, s67, v205
	v_mov_b32_e32 v130, v187
	v_med3_f32 v16, v16, s67, v205
	v_med3_f32 v17, v17, s67, v205
	v_mov_b32_e32 v131, v187
	v_cvt_pk_fp8_f32 v133, v8, v9 op_sel:[0,0,1]
	v_cvt_pk_fp8_f32 v134, v6, v7 op_sel:[0,0,1]
	v_med3_f32 v8, v2, s67, v205
	ds_read_b128 v[0:3], v214
	ds_read_b128 v[4:7], v214 offset:16
	s_lshl_b32 s75, s17, 8
	s_ashr_i32 s3, s2, 31
	v_cvt_pk_fp8_f32 v120, v62, v63 op_sel:[0,0,1]
	v_cvt_pk_fp8_f32 v121, v56, v57 op_sel:[0,0,1]
	v_cvt_pk_fp8_f32 v122, v54, v55 op_sel:[0,0,1]
	v_cvt_pk_fp8_f32 v123, v48, v49 op_sel:[0,0,1]
	v_cvt_pk_fp8_f32 v124, v46, v47 op_sel:[0,0,1]
	v_cvt_pk_fp8_f32 v125, v40, v41 op_sel:[0,0,1]
	v_cvt_pk_fp8_f32 v126, v38, v39 op_sel:[0,0,1]
	v_cvt_pk_fp8_f32 v127, v32, v33 op_sel:[0,0,1]
	v_cvt_pk_fp8_f32 v128, v28, v29
	v_cvt_pk_fp8_f32 v129, v24, v25
	v_cvt_pk_fp8_f32 v130, v20, v21
	v_cvt_pk_fp8_f32 v131, v16, v17
	s_addk_i32 s75, 0x2000
	s_lshl_b64 s[2:3], s[2:3], 16
	v_max_f32_e32 v9, v73, v73
	s_add_u32 s2, s40, s2
	v_med3_f32 v9, v9, s67, v205
	s_addc_u32 s3, s41, s3
	v_med3_f32 v30, v30, s67, v205
	v_med3_f32 v31, v31, s67, v205
	v_med3_f32 v24, v26, s67, v205
	v_med3_f32 v25, v27, s67, v205
	v_med3_f32 v22, v22, s67, v205
	v_med3_f32 v23, v23, s67, v205
	v_med3_f32 v16, v18, s67, v205
	v_med3_f32 v17, v19, s67, v205
	v_cvt_pk_fp8_f32 v143, v8, v9 op_sel:[0,0,1]
	v_lshl_add_u64 v[8:9], s[2:3], 0, v[102:103]
	v_cvt_pk_fp8_f32 v128, v30, v31 op_sel:[0,0,1]
	v_cvt_pk_fp8_f32 v129, v24, v25 op_sel:[0,0,1]
	v_cvt_pk_fp8_f32 v130, v22, v23 op_sel:[0,0,1]
	v_cvt_pk_fp8_f32 v131, v16, v17 op_sel:[0,0,1]
	s_waitcnt lgkmcnt(0)
	v_mfma_scale_f32_32x32x64_f8f6f4 v[16:31], v[0:7], v[120:127], 0, v207, v207 op_sel_hi:[0,0,0]
	ds_read_b128 v[0:3], v214 offset:64
	ds_read_b128 v[4:7], v214 offset:80
	global_load_dwordx4 v[172:175], v[8:9], off
	v_med3_f32 v12, v12, s67, v205
	v_med3_f32 v13, v13, s67, v205
	v_mov_b32_e32 v132, v187
	v_cvt_pk_fp8_f32 v132, v12, v13
	v_med3_f32 v14, v14, s67, v205
	v_med3_f32 v15, v15, s67, v205
	s_mov_b32 s17, s16
	v_cvt_pk_fp8_f32 v132, v14, v15 op_sel:[0,0,1]
	s_mov_b32 s18, s16
	s_mov_b32 s19, s16
	s_mov_b32 s20, s16
	s_mov_b32 s21, s16
	s_mov_b32 s22, s16
	s_waitcnt lgkmcnt(0)
	v_mfma_scale_f32_32x32x64_f8f6f4 v[16:31], v[0:7], v[128:135], v[16:31], v207, v207 op_sel_hi:[0,0,0]
	v_sub_u32_e32 v0, v214, v108
	ds_read_b128 v[32:35], v0 offset:128
	ds_read_b128 v[36:39], v0 offset:160
	s_mov_b32 s23, s16
	s_mov_b32 s24, s16
	s_mov_b32 s25, s16
	s_mov_b32 s26, s16
	s_mov_b32 s27, s16
	s_mov_b32 s28, s16
	s_mov_b32 s29, s16
	s_mov_b32 s30, s16
	s_mov_b32 s31, s16
	v_mov_b64_e32 v[0:1], s[16:17]
	v_and_b32_e32 v64, 63, v109
	v_mov_b64_e32 v[14:15], s[30:31]
	v_mov_b64_e32 v[2:3], s[18:19]
	s_waitcnt lgkmcnt(0)
	v_mfma_scale_f32_32x32x64_f8f6f4 v[16:31], v[32:39], v[136:143], v[16:31], v207, v207 op_sel_hi:[0,0,0]
	v_mov_b64_e32 v[4:5], s[20:21]
	v_mov_b64_e32 v[6:7], s[22:23]
	v_mov_b64_e32 v[8:9], s[24:25]
	v_mov_b64_e32 v[10:11], s[26:27]
	v_mov_b64_e32 v[12:13], s[28:29]
	v_mov_b32_e32 v112, 0x38383838
	v_cmp_gt_u32_e64 s[2:3], 32, v64
	v_mov_b64_e32 v[62:63], v[14:15]
	v_mov_b64_e32 v[78:79], v[14:15]
	s_mov_b32 s76, 2
	v_sub_u32_e32 v215, 0, v108
	v_lshl_add_u32 v208, v188, 2, s77
	v_mov_b32_e32 v113, v112
	v_mov_b32_e32 v114, v112
	s_nop 5
	v_max_f32_e32 v32, v16, v17
	v_max3_f32 v32, v32, v18, v19
	v_max3_f32 v32, v32, v20, v21
	v_max3_f32 v32, v32, v22, v23
	v_max3_f32 v32, v32, v24, v25
	v_max3_f32 v32, v32, v26, v27
	v_max3_f32 v32, v32, v28, v29
	v_max3_f32 v32, v32, v30, v31
	v_mov_b32_e32 v33, v32
	s_nop 1
	v_permlane32_swap_b32_e32 v32, v33
	v_max_f32_e32 v32, v32, v33
	v_fmamk_f32 v33, v32, 0x3dd53b94, v203
	v_fmamk_f32 v32, v32, 0x3dd53b94, v204
	v_max_f32_e32 v32, 0xf149f2ca, v32
	v_cmp_ge_f32_e32 vcc, s68, v33
	v_sub_f32_e32 v33, 0xf149f2ca, v32
	s_cmp_eq_u64 vcc, exec
	v_exp_f32_e32 v33, v33
	s_cselect_b64 vcc, -1, 0
	v_cndmask_b32_e32 v194, v32, v206, vcc
	v_pk_fma_f32 v[178:179], v[16:17], s[38:39], v[194:195] op_sel_hi:[1,0,0] neg_lo:[0,0,1] neg_hi:[0,0,1]
	v_mul_u32_u24_e32 v16, 0x50, v188
	v_pk_fma_f32 v[152:153], v[30:31], s[38:39], v[194:195] op_sel_hi:[1,0,0] neg_lo:[0,0,1] neg_hi:[0,0,1]
	v_pk_fma_f32 v[154:155], v[28:29], s[38:39], v[194:195] op_sel_hi:[1,0,0] neg_lo:[0,0,1] neg_hi:[0,0,1]
	v_pk_fma_f32 v[156:157], v[26:27], s[38:39], v[194:195] op_sel_hi:[1,0,0] neg_lo:[0,0,1] neg_hi:[0,0,1]
	v_pk_fma_f32 v[158:159], v[24:25], s[38:39], v[194:195] op_sel_hi:[1,0,0] neg_lo:[0,0,1] neg_hi:[0,0,1]
	v_pk_fma_f32 v[160:161], v[22:23], s[38:39], v[194:195] op_sel_hi:[1,0,0] neg_lo:[0,0,1] neg_hi:[0,0,1]
	v_pk_fma_f32 v[162:163], v[20:21], s[38:39], v[194:195] op_sel_hi:[1,0,0] neg_lo:[0,0,1] neg_hi:[0,0,1]
	v_pk_fma_f32 v[176:177], v[18:19], s[38:39], v[194:195] op_sel_hi:[1,0,0] neg_lo:[0,0,1] neg_hi:[0,0,1]
	v_cndmask_b32_e64 v88, v33, 1.0, vcc
	v_add3_u32 v209, s65, v16, v186
	v_mov_b64_e32 v[30:31], v[14:15]
	v_mov_b64_e32 v[46:47], v[14:15]
	v_mov_b32_e32 v115, v112
	v_mov_b32_e32 v116, v112
	v_mov_b32_e32 v117, v112
	v_mov_b32_e32 v118, v112
	v_mov_b32_e32 v119, v112
	v_lshlrev_b32_e32 v186, 2, v107
	v_mul_lo_u32 v216, v212, s63
	v_lshl_add_u32 v213, v107, 4, s77
	v_lshl_add_u64 v[196:197], s[4:5], 0, v[190:191]
	v_lshl_add_u64 v[198:199], s[4:5], 0, v[192:193]
	v_lshl_add_u64 v[200:201], s[40:41], 0, v[102:103]
	s_mov_b32 s17, 0
	v_mov_b64_e32 v[28:29], v[12:13]
	v_mov_b64_e32 v[26:27], v[10:11]
	v_mov_b64_e32 v[24:25], v[8:9]
	v_mov_b64_e32 v[22:23], v[6:7]
	v_mov_b64_e32 v[20:21], v[4:5]
	v_mov_b64_e32 v[18:19], v[2:3]
	v_mov_b64_e32 v[16:17], v[0:1]
	v_mov_b64_e32 v[44:45], v[12:13]
	v_mov_b64_e32 v[42:43], v[10:11]
	v_mov_b64_e32 v[40:41], v[8:9]
	v_mov_b64_e32 v[38:39], v[6:7]
	v_mov_b64_e32 v[36:37], v[4:5]
	v_mov_b64_e32 v[34:35], v[2:3]
	v_mov_b64_e32 v[32:33], v[0:1]
	v_mov_b64_e32 v[60:61], v[12:13]
	v_mov_b64_e32 v[58:59], v[10:11]
	v_mov_b64_e32 v[56:57], v[8:9]
	v_mov_b64_e32 v[54:55], v[6:7]
	v_mov_b64_e32 v[52:53], v[4:5]
	v_mov_b64_e32 v[50:51], v[2:3]
	v_mov_b64_e32 v[48:49], v[0:1]
	v_mov_b64_e32 v[76:77], v[12:13]
	v_mov_b64_e32 v[74:75], v[10:11]
	v_mov_b64_e32 v[72:73], v[8:9]
	v_mov_b64_e32 v[70:71], v[6:7]
	v_mov_b64_e32 v[68:69], v[4:5]
	v_mov_b64_e32 v[66:67], v[2:3]
	v_mov_b64_e32 v[64:65], v[0:1]
	s_branch .LBB0_1876

.LBB0_1893:
	s_waitcnt lgkmcnt(4)
	v_mfma_scale_f32_32x32x64_f8f6f4 v[80:95], v[80:87], v[120:127], 0, v207, v207 op_sel_hi:[0,0,0]
	v_exp_f32_e32 v120, v153
	s_waitcnt lgkmcnt(0)
	s_barrier
	v_mfma_scale_f32_32x32x64_f8f6f4 v[80:95], v[104:111], v[128:135], v[80:95], v207, v207 op_sel_hi:[0,0,0]
	v_exp_f32_e32 v105, v158
	v_exp_f32_e32 v106, v159
	v_exp_f32_e32 v109, v154
	v_exp_f32_e32 v110, v155
	v_exp_f32_e32 v104, v161
	v_exp_f32_e32 v107, v156
	v_exp_f32_e32 v108, v157
	v_exp_f32_e32 v111, v152
	v_mfma_scale_f32_32x32x64_f8f6f4 v[80:95], v[96:103], v[136:143], v[80:95], v207, v207 op_sel_hi:[0,0,0]
	v_exp_f32_e32 v97, v178
	v_exp_f32_e32 v98, v179
	v_mov_b32_e32 v96, v187
	v_exp_f32_e32 v100, v176
	v_exp_f32_e32 v101, v177
	v_cvt_pk_fp8_f32 v96, v97, v98
	v_exp_f32_e32 v99, v162
	v_exp_f32_e32 v102, v163
	v_mov_b32_e32 v97, v187
	v_cvt_pk_fp8_f32 v96, v100, v101 op_sel:[0,0,1]
	v_mov_b32_e32 v98, v187
	v_cvt_pk_fp8_f32 v97, v99, v102
	v_mov_b32_e32 v99, v187
	v_max_f32_e32 v102, v194, v194
	v_exp_f32_e32 v103, v160
	s_nop 4
	v_max_f32_e32 v100, v80, v81
	v_max3_f32 v100, v100, v82, v83
	v_max3_f32 v100, v100, v84, v85
	v_max3_f32 v100, v100, v86, v87
	v_max3_f32 v100, v100, v88, v89
	v_max3_f32 v100, v100, v90, v91
	v_max3_f32 v100, v100, v92, v93
	v_max3_f32 v100, v100, v94, v95
	v_mov_b32_e32 v101, v100
	s_nop 1
	v_permlane32_swap_b32_e32 v100, v101
	v_max_f32_e32 v100, v100, v101
	v_fma_f32 v101, v100, s38, -v194
	v_fmamk_f32 v100, v100, 0x3dd53b94, v204
	v_cvt_pk_fp8_f32 v98, v105, v106
	v_cvt_pk_fp8_f32 v99, v109, v110
	v_max_f32_e32 v124, v102, v100
	v_sub_f32_e32 v100, v194, v124
	v_exp_f32_e32 v100, v100
	v_cmp_ge_f32_e32 vcc, s68, v101
	v_cvt_pk_fp8_f32 v97, v103, v104 op_sel:[0,0,1]
	v_cvt_pk_fp8_f32 v98, v107, v108 op_sel:[0,0,1]
	v_cvt_pk_fp8_f32 v99, v111, v120 op_sel:[0,0,1]
	s_cmp_eq_u64 vcc, exec
	s_cselect_b64 s[0:1], -1, 0
	v_cndmask_b32_e64 v125, v100, 1.0, s[0:1]
	v_cmp_gt_f32_e32 vcc, 1.0, v125
	s_cbranch_vccz .LBB0_1897
	s_and_saveexec_b64 s[4:5], s[2:3]
	ds_write_b32 v208, v125 offset:128
	s_or_b64 exec, exec, s[4:5]
	v_cvt_f32_fp8_e32 v126, v96
	v_cvt_f32_fp8_sdwa v127, v96 src0_sel:BYTE_1
	v_cvt_f32_fp8_sdwa v128, v96 src0_sel:BYTE_2
	v_cvt_f32_fp8_sdwa v96, v96 src0_sel:BYTE_3
	v_mul_f32_e32 v126, v125, v126
	v_mul_f32_e32 v127, v125, v127
	v_med3_f32 v126, v126, s67, v205
	v_mul_f32_e32 v96, v125, v96
	v_med3_f32 v127, v127, s67, v205
	v_med3_f32 v129, v96, s67, v205
	v_mov_b32_e32 v96, v187
	v_cvt_pk_fp8_f32 v96, v126, v127
	v_cvt_f32_fp8_e32 v126, v97
	v_cvt_f32_fp8_sdwa v127, v97 src0_sel:BYTE_1
	v_mul_f32_e32 v128, v125, v128
	v_med3_f32 v128, v128, s67, v205
	v_cvt_f32_fp8_sdwa v130, v97 src0_sel:BYTE_2
	v_cvt_pk_fp8_f32 v96, v128, v129 op_sel:[0,0,1]
	v_mul_f32_e32 v126, v125, v126
	v_mul_f32_e32 v127, v125, v127
	v_cvt_f32_fp8_sdwa v129, v97 src0_sel:BYTE_3
	v_med3_f32 v126, v126, s67, v205
	v_med3_f32 v127, v127, s67, v205
	v_mov_b32_e32 v97, v187
	v_cvt_pk_fp8_f32 v97, v126, v127
	v_mul_f32_e32 v128, v125, v130
	v_mul_f32_e32 v126, v125, v129
	v_med3_f32 v127, v128, s67, v205
	v_med3_f32 v126, v126, s67, v205
	v_cvt_pk_fp8_f32 v97, v127, v126 op_sel:[0,0,1]
	v_cvt_f32_fp8_e32 v126, v98
	v_cvt_f32_fp8_sdwa v127, v98 src0_sel:BYTE_1
	v_cvt_f32_fp8_sdwa v128, v98 src0_sel:BYTE_2
	v_cvt_f32_fp8_sdwa v98, v98 src0_sel:BYTE_3
	v_mul_f32_e32 v126, v125, v126
	v_mul_f32_e32 v127, v125, v127
	v_med3_f32 v126, v126, s67, v205
	v_mul_f32_e32 v98, v125, v98
	v_med3_f32 v127, v127, s67, v205
	v_med3_f32 v129, v98, s67, v205
	v_mov_b32_e32 v98, v187
	v_cvt_pk_fp8_f32 v98, v126, v127
	v_cvt_f32_fp8_e32 v126, v99
	v_cvt_f32_fp8_sdwa v127, v99 src0_sel:BYTE_1
	v_mul_f32_e32 v128, v125, v128
	v_med3_f32 v128, v128, s67, v205
	v_cvt_f32_fp8_sdwa v130, v99 src0_sel:BYTE_2
	v_cvt_pk_fp8_f32 v98, v128, v129 op_sel:[0,0,1]
	v_mul_f32_e32 v126, v125, v126
	v_mul_f32_e32 v127, v125, v127
	v_cvt_f32_fp8_sdwa v129, v99 src0_sel:BYTE_3
	v_med3_f32 v126, v126, s67, v205
	v_med3_f32 v127, v127, s67, v205
	v_mov_b32_e32 v99, v187
	v_cvt_pk_fp8_f32 v99, v126, v127
	s_waitcnt lgkmcnt(0)
	ds_read_b128 v[120:123], v213 offset:224
	ds_read_b128 v[108:111], v213 offset:192
	ds_read_b128 v[104:107], v213 offset:160
	ds_read_b128 v[100:103], v213 offset:128
	v_mul_f32_e32 v128, v125, v130
	v_mul_f32_e32 v125, v125, v129
	v_med3_f32 v126, v128, s67, v205
	v_med3_f32 v125, v125, s67, v205
	v_cvt_pk_fp8_f32 v99, v126, v125 op_sel:[0,0,1]
	s_waitcnt lgkmcnt(3)
	v_pk_mul_f32 v[62:63], v[62:63], v[122:123]
	s_waitcnt lgkmcnt(2)
	v_pk_mul_f32 v[58:59], v[58:59], v[110:111]
	s_waitcnt lgkmcnt(1)
	v_pk_mul_f32 v[54:55], v[54:55], v[106:107]
	s_waitcnt lgkmcnt(0)
	v_pk_mul_f32 v[50:51], v[50:51], v[102:103]
	v_pk_mul_f32 v[60:61], v[60:61], v[120:121]
	v_pk_mul_f32 v[56:57], v[56:57], v[108:109]
	v_pk_mul_f32 v[52:53], v[52:53], v[104:105]
	v_pk_mul_f32 v[48:49], v[48:49], v[100:101]
	v_pk_mul_f32 v[46:47], v[46:47], v[122:123]
	v_pk_mul_f32 v[42:43], v[42:43], v[110:111]
	v_pk_mul_f32 v[38:39], v[38:39], v[106:107]
	v_pk_mul_f32 v[34:35], v[34:35], v[102:103]
	v_pk_mul_f32 v[44:45], v[44:45], v[120:121]
	v_pk_mul_f32 v[40:41], v[40:41], v[108:109]
	v_pk_mul_f32 v[36:37], v[36:37], v[104:105]
	v_pk_mul_f32 v[32:33], v[32:33], v[100:101]
	v_pk_mul_f32 v[30:31], v[30:31], v[122:123]
	v_pk_mul_f32 v[26:27], v[26:27], v[110:111]
	v_pk_mul_f32 v[22:23], v[22:23], v[106:107]
	v_pk_mul_f32 v[18:19], v[18:19], v[102:103]
	v_pk_mul_f32 v[28:29], v[28:29], v[120:121]
	v_pk_mul_f32 v[24:25], v[24:25], v[108:109]
	v_pk_mul_f32 v[20:21], v[20:21], v[104:105]
	v_pk_mul_f32 v[16:17], v[16:17], v[100:101]
	v_pk_mul_f32 v[14:15], v[14:15], v[122:123]
	v_pk_mul_f32 v[10:11], v[10:11], v[110:111]
	v_pk_mul_f32 v[6:7], v[6:7], v[106:107]
	v_pk_mul_f32 v[2:3], v[2:3], v[102:103]
	v_pk_mul_f32 v[12:13], v[12:13], v[120:121]
	v_pk_mul_f32 v[8:9], v[8:9], v[108:109]
	v_pk_mul_f32 v[4:5], v[4:5], v[104:105]
	v_pk_mul_f32 v[0:1], v[0:1], v[100:101]
	v_pk_mul_f32 v[78:79], v[78:79], v[122:123]
	v_pk_mul_f32 v[74:75], v[74:75], v[110:111]
	v_pk_mul_f32 v[70:71], v[70:71], v[106:107]
	v_pk_mul_f32 v[66:67], v[66:67], v[102:103]
	v_pk_mul_f32 v[76:77], v[76:77], v[120:121]
	v_pk_mul_f32 v[72:73], v[72:73], v[108:109]
	v_pk_mul_f32 v[68:69], v[68:69], v[104:105]
	v_pk_mul_f32 v[64:65], v[64:65], v[100:101]

.LBB0_1919:
	s_nop 8
	v_max_f32_e32 v48, v32, v33
	v_max3_f32 v48, v48, v34, v35
	v_max3_f32 v48, v48, v36, v37
	v_max3_f32 v48, v48, v38, v39
	v_max3_f32 v48, v48, v40, v41
	v_max3_f32 v48, v48, v42, v43
	v_max3_f32 v48, v48, v44, v45
	v_max3_f32 v48, v48, v46, v47
	v_mov_b32_e32 v49, v48
	s_nop 1
	v_permlane32_swap_b32_e32 v48, v49
	v_max_f32_e32 v48, v48, v49
	v_sub_f32_e32 v49, v48, v130
	v_cmp_ge_f32_e32 vcc, s50, v49
	s_cmp_eq_u64 vcc, exec
	v_max_f32_e32 v48, v130, v48
	s_cselect_b64 vcc, -1, 0
	v_sub_f32_e32 v49, v130, v48
	v_cndmask_b32_e32 v130, v48, v130, vcc
	v_sub_f32_e32 v32, v32, v130
	v_exp_f32_e32 v32, v32
	v_sub_f32_e32 v33, v33, v130
	v_exp_f32_e32 v33, v33
	v_sub_f32_e32 v34, v34, v130
	v_exp_f32_e32 v34, v34
	v_sub_f32_e32 v35, v35, v130
	v_exp_f32_e32 v35, v35
	v_sub_f32_e32 v36, v36, v130
	v_exp_f32_e32 v36, v36
	v_sub_f32_e32 v37, v37, v130
	v_add_f32_e32 v48, 0, v32
	v_exp_f32_e32 v37, v37
	v_sub_f32_e32 v38, v38, v130
	v_add_f32_e32 v48, v33, v48
	v_exp_f32_e32 v38, v38
	v_sub_f32_e32 v39, v39, v130
	v_add_f32_e32 v48, v34, v48
	v_exp_f32_e32 v39, v39
	v_sub_f32_e32 v40, v40, v130
	v_add_f32_e32 v48, v35, v48
	v_exp_f32_e32 v40, v40
	v_sub_f32_e32 v41, v41, v130
	v_add_f32_e32 v48, v36, v48
	v_exp_f32_e32 v41, v41
	v_sub_f32_e32 v42, v42, v130
	v_add_f32_e32 v48, v37, v48
	v_exp_f32_e32 v42, v42
	v_sub_f32_e32 v43, v43, v130
	v_add_f32_e32 v48, v38, v48
	v_exp_f32_e32 v43, v43
	v_sub_f32_e32 v44, v44, v130
	v_add_f32_e32 v48, v39, v48
	v_exp_f32_e32 v44, v44
	v_sub_f32_e32 v45, v45, v130
	v_add_f32_e32 v48, v40, v48
	v_exp_f32_e32 v45, v45
	v_sub_f32_e32 v46, v46, v130
	v_add_f32_e32 v48, v41, v48
	v_exp_f32_e32 v46, v46
	v_sub_f32_e32 v47, v47, v130
	v_add_f32_e32 v48, v42, v48
	v_exp_f32_e32 v47, v47
	v_add_f32_e32 v48, v43, v48
	v_exp_f32_e32 v49, v49
	v_add_f32_e32 v48, v44, v48
	v_add_f32_e32 v48, v45, v48
	v_add_f32_e32 v48, v46, v48
	v_add_f32_e32 v132, v47, v48
	v_cndmask_b32_e64 v131, v49, 1.0, vcc
	v_mov_b32_e32 v133, v132
	v_cvt_pk_bf16_f32 v32, v32, v33
	v_cvt_pk_bf16_f32 v33, v34, v35
	v_cvt_pk_bf16_f32 v34, v36, v37
	v_cvt_pk_bf16_f32 v35, v38, v39
	v_cvt_pk_bf16_f32 v36, v40, v41
	v_cvt_pk_bf16_f32 v37, v42, v43
	v_cvt_pk_bf16_f32 v38, v44, v45
	v_cvt_pk_bf16_f32 v39, v46, v47
	s_nop 1
	v_permlane32_swap_b32_e32 v132, v133
	v_permlane32_swap_b32_e32 v32, v34
	v_permlane32_swap_b32_e32 v33, v35
	v_permlane32_swap_b32_e32 v36, v38
	v_permlane32_swap_b32_e32 v37, v39
	v_cmp_gt_f32_e32 vcc, 1.0, v131
	s_cbranch_vccz .LBB0_1923
	s_and_saveexec_b64 s[18:19], s[0:1]
	ds_write_b32 v117, v131 offset:128
	s_or_b64 exec, exec, s[18:19]
	s_waitcnt lgkmcnt(0)
	ds_read_b128 v[40:43], v126 offset:224
	ds_read_b128 v[44:47], v126 offset:192
	ds_read_b128 v[48:51], v126 offset:160
	ds_read_b128 v[52:55], v126 offset:128
	s_waitcnt lgkmcnt(3)
	v_pk_mul_f32 v[14:15], v[14:15], v[42:43]
	s_waitcnt lgkmcnt(2)
	v_pk_mul_f32 v[10:11], v[10:11], v[46:47]
	s_waitcnt lgkmcnt(1)
	v_pk_mul_f32 v[6:7], v[6:7], v[50:51]
	s_waitcnt lgkmcnt(0)
	v_pk_mul_f32 v[2:3], v[2:3], v[54:55]
	v_pk_mul_f32 v[30:31], v[30:31], v[42:43]
	v_pk_mul_f32 v[26:27], v[26:27], v[46:47]
	v_pk_mul_f32 v[22:23], v[22:23], v[50:51]
	v_pk_mul_f32 v[18:19], v[18:19], v[54:55]
	v_pk_mul_f32 v[12:13], v[12:13], v[40:41]
	v_pk_mul_f32 v[8:9], v[8:9], v[44:45]
	v_pk_mul_f32 v[4:5], v[4:5], v[48:49]
	v_pk_mul_f32 v[0:1], v[0:1], v[52:53]
	v_pk_mul_f32 v[28:29], v[28:29], v[40:41]
	v_pk_mul_f32 v[24:25], v[24:25], v[44:45]
	v_pk_mul_f32 v[20:21], v[20:21], v[48:49]
	v_pk_mul_f32 v[16:17], v[16:17], v[52:53]

.LBB0_1927:
	s_nop 8
	v_max_f32_e32 v32, v48, v49
	v_max3_f32 v32, v32, v50, v51
	v_max3_f32 v32, v32, v52, v53
	v_max3_f32 v32, v32, v54, v55
	v_max3_f32 v32, v32, v56, v57
	v_max3_f32 v32, v32, v58, v59
	v_max3_f32 v32, v32, v60, v61
	v_max3_f32 v32, v32, v62, v63
	v_mov_b32_e32 v33, v32
	s_nop 1
	v_permlane32_swap_b32_e32 v32, v33
	v_max_f32_e32 v32, v32, v33
	v_sub_f32_e32 v33, v32, v130
	v_cmp_ge_f32_e32 vcc, s50, v33
	s_cmp_eq_u64 vcc, exec
	v_max_f32_e32 v32, v130, v32
	s_cselect_b64 vcc, -1, 0
	v_sub_f32_e32 v33, v130, v32
	v_cndmask_b32_e32 v130, v32, v130, vcc
	v_sub_f32_e32 v40, v55, v130
	v_exp_f32_e32 v43, v40
	v_sub_f32_e32 v40, v56, v130
	v_exp_f32_e32 v44, v40
	v_sub_f32_e32 v40, v57, v130
	v_exp_f32_e32 v45, v40
	v_sub_f32_e32 v40, v58, v130
	v_sub_f32_e32 v32, v48, v130
	v_exp_f32_e32 v46, v40
	v_sub_f32_e32 v40, v59, v130
	v_exp_f32_e32 v32, v32
	v_sub_f32_e32 v34, v49, v130
	v_exp_f32_e32 v47, v40
	v_sub_f32_e32 v40, v60, v130
	v_exp_f32_e32 v34, v34
	v_sub_f32_e32 v35, v50, v130
	v_exp_f32_e32 v48, v40
	v_sub_f32_e32 v40, v61, v130
	v_exp_f32_e32 v35, v35
	v_sub_f32_e32 v36, v51, v130
	v_exp_f32_e32 v49, v40
	v_sub_f32_e32 v40, v62, v130
	v_exp_f32_e32 v36, v36
	v_sub_f32_e32 v37, v52, v130
	v_exp_f32_e32 v50, v40
	v_sub_f32_e32 v40, v63, v130
	v_exp_f32_e32 v37, v37
	v_sub_f32_e32 v38, v53, v130
	v_exp_f32_e32 v51, v40
	v_add_f32_e32 v40, 0, v32
	v_exp_f32_e32 v38, v38
	v_sub_f32_e32 v39, v54, v130
	v_add_f32_e32 v40, v34, v40
	v_exp_f32_e32 v39, v39
	v_add_f32_e32 v40, v35, v40
	v_add_f32_e32 v40, v36, v40
	v_add_f32_e32 v40, v37, v40
	v_add_f32_e32 v40, v38, v40
	v_add_f32_e32 v40, v39, v40
	v_add_f32_e32 v40, v43, v40
	v_add_f32_e32 v40, v44, v40
	v_add_f32_e32 v40, v45, v40
	v_add_f32_e32 v40, v46, v40
	v_add_f32_e32 v40, v47, v40
	v_exp_f32_e32 v33, v33
	v_add_f32_e32 v40, v48, v40
	v_add_f32_e32 v40, v49, v40
	v_add_f32_e32 v40, v50, v40
	v_add_f32_e32 v41, v51, v40
	v_cndmask_b32_e64 v40, v33, 1.0, vcc
	v_mov_b32_e32 v42, v41
	v_cvt_pk_bf16_f32 v32, v32, v34
	v_cvt_pk_bf16_f32 v33, v35, v36
	v_cvt_pk_bf16_f32 v34, v37, v38
	v_cvt_pk_bf16_f32 v35, v39, v43
	v_cvt_pk_bf16_f32 v36, v44, v45
	v_cvt_pk_bf16_f32 v37, v46, v47
	v_cvt_pk_bf16_f32 v38, v48, v49
	v_cvt_pk_bf16_f32 v39, v50, v51
	s_nop 1
	v_permlane32_swap_b32_e32 v41, v42
	v_permlane32_swap_b32_e32 v32, v34
	v_permlane32_swap_b32_e32 v33, v35
	v_permlane32_swap_b32_e32 v36, v38
	v_permlane32_swap_b32_e32 v37, v39
	v_cmp_gt_f32_e32 vcc, 1.0, v40
	s_cbranch_vccz .LBB0_1931
	s_and_saveexec_b64 s[16:17], s[0:1]
	ds_write_b32 v117, v40 offset:128
	s_or_b64 exec, exec, s[16:17]
	s_waitcnt lgkmcnt(0)
	ds_read_b128 v[44:47], v126 offset:224
	ds_read_b128 v[48:51], v126 offset:192
	ds_read_b128 v[52:55], v126 offset:160
	ds_read_b128 v[56:59], v126 offset:128
	s_waitcnt lgkmcnt(3)
	v_pk_mul_f32 v[30:31], v[30:31], v[46:47]
	s_waitcnt lgkmcnt(2)
	v_pk_mul_f32 v[26:27], v[26:27], v[50:51]
	s_waitcnt lgkmcnt(1)
	v_pk_mul_f32 v[22:23], v[22:23], v[54:55]
	s_waitcnt lgkmcnt(0)
	v_pk_mul_f32 v[18:19], v[18:19], v[58:59]
	v_pk_mul_f32 v[28:29], v[28:29], v[44:45]
	v_pk_mul_f32 v[24:25], v[24:25], v[48:49]
	v_pk_mul_f32 v[20:21], v[20:21], v[52:53]
	v_pk_mul_f32 v[16:17], v[16:17], v[56:57]
	v_pk_mul_f32 v[14:15], v[14:15], v[46:47]
	v_pk_mul_f32 v[10:11], v[10:11], v[50:51]
	v_pk_mul_f32 v[6:7], v[6:7], v[54:55]
	v_pk_mul_f32 v[2:3], v[2:3], v[58:59]
	v_pk_mul_f32 v[12:13], v[12:13], v[44:45]
	v_pk_mul_f32 v[8:9], v[8:9], v[48:49]
	v_pk_mul_f32 v[4:5], v[4:5], v[52:53]
	v_pk_mul_f32 v[0:1], v[0:1], v[56:57]

.LBB0_2077:
	v_max_f32_e32 v14, v82, v83
	v_max3_f32 v14, v14, v84, v85
	v_max3_f32 v14, v14, v86, v87
	v_max3_f32 v14, v14, v88, v89
	v_max3_f32 v14, v14, v90, v91
	v_max3_f32 v14, v14, v92, v93
	v_max3_f32 v14, v14, v94, v95
	v_max3_f32 v14, v14, v96, v97
	v_mov_b32_e32 v15, v14
	s_nop 1
	v_permlane32_swap_b32_e32 v14, v15
	v_max_f32_e32 v14, v14, v15
	v_sub_f32_e32 v15, v14, v244
	v_cmp_ge_f32_e32 vcc, s61, v15
	s_cmp_eq_u64 vcc, exec
	v_max_f32_e32 v14, v244, v14
	s_cselect_b64 vcc, -1, 0
	v_sub_f32_e32 v15, v244, v14
	v_cndmask_b32_e32 v244, v14, v244, vcc
	v_sub_f32_e32 v14, v82, v244
	v_exp_f32_e32 v82, v14
	v_sub_f32_e32 v14, v83, v244
	v_exp_f32_e32 v83, v14
	v_sub_f32_e32 v14, v84, v244
	v_exp_f32_e32 v84, v14
	v_sub_f32_e32 v14, v85, v244
	v_exp_f32_e32 v85, v14
	v_sub_f32_e32 v14, v86, v244
	v_exp_f32_e32 v86, v14
	v_sub_f32_e32 v14, v87, v244
	v_exp_f32_e32 v87, v14
	v_sub_f32_e32 v14, v88, v244
	v_exp_f32_e32 v88, v14
	v_sub_f32_e32 v14, v89, v244
	v_exp_f32_e32 v89, v14
	v_sub_f32_e32 v14, v90, v244
	v_exp_f32_e32 v90, v14
	v_sub_f32_e32 v14, v91, v244
	v_exp_f32_e32 v91, v14
	v_sub_f32_e32 v14, v92, v244
	v_exp_f32_e32 v92, v14
	v_sub_f32_e32 v14, v93, v244
	v_exp_f32_e32 v93, v14
	v_sub_f32_e32 v14, v94, v244
	v_exp_f32_e32 v94, v14
	v_sub_f32_e32 v14, v95, v244
	v_exp_f32_e32 v95, v14
	v_sub_f32_e32 v14, v96, v244
	v_exp_f32_e32 v96, v14
	v_sub_f32_e32 v14, v97, v244
	v_exp_f32_e32 v97, v14
	v_add_f32_e32 v14, 0, v82
	v_add_f32_e32 v14, v83, v14
	v_add_f32_e32 v14, v84, v14
	v_add_f32_e32 v14, v85, v14
	v_add_f32_e32 v14, v86, v14
	v_add_f32_e32 v14, v87, v14
	v_add_f32_e32 v14, v88, v14
	v_add_f32_e32 v14, v89, v14
	v_add_f32_e32 v14, v90, v14
	v_add_f32_e32 v14, v91, v14
	v_add_f32_e32 v14, v92, v14
	v_add_f32_e32 v14, v93, v14
	v_exp_f32_e32 v98, v15
	v_add_f32_e32 v14, v94, v14
	v_add_f32_e32 v14, v95, v14
	v_add_f32_e32 v14, v96, v14
	v_add_f32_e32 v15, v97, v14
	v_cndmask_b32_e64 v14, v98, 1.0, vcc
	v_mov_b32_e32 v243, v15
	v_cvt_pk_bf16_f32 v82, v82, v83
	v_cvt_pk_bf16_f32 v83, v84, v85
	v_cvt_pk_bf16_f32 v84, v86, v87
	v_cvt_pk_bf16_f32 v85, v88, v89
	v_cvt_pk_bf16_f32 v86, v90, v91
	v_cvt_pk_bf16_f32 v87, v92, v93
	v_cvt_pk_bf16_f32 v88, v94, v95
	v_cvt_pk_bf16_f32 v89, v96, v97
	s_nop 1
	v_permlane32_swap_b32_e32 v15, v243
	v_permlane32_swap_b32_e32 v82, v84
	v_permlane32_swap_b32_e32 v83, v85
	v_permlane32_swap_b32_e32 v86, v88
	v_permlane32_swap_b32_e32 v87, v89
	v_cmp_gt_f32_e32 vcc, 1.0, v14
	s_cbranch_vccz .LBB0_2081
	s_and_saveexec_b64 s[16:17], s[10:11]
	ds_write_b32 v196, v14 offset:128
	s_or_b64 exec, exec, s[16:17]
	s_waitcnt lgkmcnt(0)
	ds_read_b128 v[90:93], v221 offset:224
	ds_read_b128 v[94:97], v221 offset:192
	ds_read_b128 v[98:101], v221 offset:160
	ds_read_b128 v[102:105], v221 offset:128
	s_waitcnt lgkmcnt(3)
	v_pk_mul_f32 v[78:79], v[78:79], v[92:93]
	s_waitcnt lgkmcnt(2)
	v_pk_mul_f32 v[74:75], v[74:75], v[96:97]
	s_waitcnt lgkmcnt(1)
	v_pk_mul_f32 v[70:71], v[70:71], v[100:101]
	s_waitcnt lgkmcnt(0)
	v_pk_mul_f32 v[66:67], v[66:67], v[104:105]
	v_pk_mul_f32 v[76:77], v[76:77], v[90:91]
	v_pk_mul_f32 v[72:73], v[72:73], v[94:95]
	v_pk_mul_f32 v[68:69], v[68:69], v[98:99]
	v_pk_mul_f32 v[64:65], v[64:65], v[102:103]
	v_pk_mul_f32 v[62:63], v[62:63], v[92:93]
	v_pk_mul_f32 v[58:59], v[58:59], v[96:97]
	v_pk_mul_f32 v[54:55], v[54:55], v[100:101]
	v_pk_mul_f32 v[50:51], v[50:51], v[104:105]
	v_pk_mul_f32 v[60:61], v[60:61], v[90:91]
	v_pk_mul_f32 v[56:57], v[56:57], v[94:95]
	v_pk_mul_f32 v[52:53], v[52:53], v[98:99]
	v_pk_mul_f32 v[48:49], v[48:49], v[102:103]
	v_pk_mul_f32 v[46:47], v[46:47], v[92:93]
	v_pk_mul_f32 v[42:43], v[42:43], v[96:97]
	v_pk_mul_f32 v[38:39], v[38:39], v[100:101]
	v_pk_mul_f32 v[34:35], v[34:35], v[104:105]
	v_pk_mul_f32 v[44:45], v[44:45], v[90:91]
	v_pk_mul_f32 v[40:41], v[40:41], v[94:95]
	v_pk_mul_f32 v[36:37], v[36:37], v[98:99]
	v_pk_mul_f32 v[32:33], v[32:33], v[102:103]
	v_pk_mul_f32 v[30:31], v[30:31], v[92:93]
	v_pk_mul_f32 v[26:27], v[26:27], v[96:97]
	v_pk_mul_f32 v[22:23], v[22:23], v[100:101]
	v_pk_mul_f32 v[18:19], v[18:19], v[104:105]
	v_pk_mul_f32 v[28:29], v[28:29], v[90:91]
	v_pk_mul_f32 v[24:25], v[24:25], v[94:95]
	v_pk_mul_f32 v[20:21], v[20:21], v[98:99]
	v_pk_mul_f32 v[16:17], v[16:17], v[102:103]

.LBB0_2117:
	s_nop 8
	v_max_f32_e32 v98, v82, v83
	v_max3_f32 v98, v98, v84, v85
	v_max3_f32 v98, v98, v86, v87
	v_max3_f32 v98, v98, v88, v89
	v_max3_f32 v98, v98, v90, v91
	v_max3_f32 v98, v98, v92, v93
	v_max3_f32 v98, v98, v94, v95
	v_max3_f32 v98, v98, v96, v97
	v_mov_b32_e32 v99, v98
	s_nop 1
	v_permlane32_swap_b32_e32 v98, v99
	v_max_f32_e32 v98, v98, v99
	v_sub_f32_e32 v99, v98, v244
	v_cmp_ge_f32_e32 vcc, s61, v99
	s_cmp_eq_u64 vcc, exec
	v_max_f32_e32 v98, v244, v98
	s_cselect_b64 vcc, -1, 0
	v_sub_f32_e32 v99, v244, v98
	v_cndmask_b32_e32 v244, v98, v244, vcc
	v_sub_f32_e32 v90, v90, v244
	v_exp_f32_e32 v98, v90
	v_sub_f32_e32 v90, v91, v244
	v_exp_f32_e32 v100, v90
	v_sub_f32_e32 v90, v92, v244
	v_sub_f32_e32 v82, v82, v244
	v_exp_f32_e32 v101, v90
	v_sub_f32_e32 v90, v93, v244
	v_exp_f32_e32 v82, v82
	v_sub_f32_e32 v83, v83, v244
	v_exp_f32_e32 v93, v90
	v_sub_f32_e32 v90, v94, v244
	v_exp_f32_e32 v83, v83
	v_sub_f32_e32 v84, v84, v244
	v_exp_f32_e32 v94, v90
	v_sub_f32_e32 v90, v95, v244
	v_exp_f32_e32 v84, v84
	v_sub_f32_e32 v85, v85, v244
	v_exp_f32_e32 v95, v90
	v_sub_f32_e32 v90, v96, v244
	v_exp_f32_e32 v85, v85
	v_sub_f32_e32 v86, v86, v244
	v_exp_f32_e32 v96, v90
	v_sub_f32_e32 v90, v97, v244
	v_exp_f32_e32 v86, v86
	v_sub_f32_e32 v87, v87, v244
	v_exp_f32_e32 v97, v90
	v_add_f32_e32 v90, 0, v82
	v_exp_f32_e32 v87, v87
	v_sub_f32_e32 v88, v88, v244
	v_add_f32_e32 v90, v83, v90
	v_exp_f32_e32 v88, v88
	v_sub_f32_e32 v89, v89, v244
	v_add_f32_e32 v90, v84, v90
	v_exp_f32_e32 v89, v89
	v_add_f32_e32 v90, v85, v90
	v_add_f32_e32 v90, v86, v90
	v_add_f32_e32 v90, v87, v90
	v_add_f32_e32 v90, v88, v90
	v_add_f32_e32 v90, v89, v90
	v_add_f32_e32 v90, v98, v90
	v_add_f32_e32 v90, v100, v90
	v_add_f32_e32 v90, v101, v90
	v_add_f32_e32 v90, v93, v90
	v_exp_f32_e32 v99, v99
	v_add_f32_e32 v90, v94, v90
	v_add_f32_e32 v90, v95, v90
	v_add_f32_e32 v90, v96, v90
	v_add_f32_e32 v91, v97, v90
	v_cndmask_b32_e64 v90, v99, 1.0, vcc
	v_mov_b32_e32 v92, v91
	v_cvt_pk_bf16_f32 v82, v82, v83
	v_cvt_pk_bf16_f32 v83, v84, v85
	v_cvt_pk_bf16_f32 v84, v86, v87
	v_cvt_pk_bf16_f32 v85, v88, v89
	v_cvt_pk_bf16_f32 v86, v98, v100
	v_cvt_pk_bf16_f32 v87, v101, v93
	v_cvt_pk_bf16_f32 v88, v94, v95
	v_cvt_pk_bf16_f32 v89, v96, v97
	s_nop 1
	v_permlane32_swap_b32_e32 v91, v92
	v_permlane32_swap_b32_e32 v82, v84
	v_permlane32_swap_b32_e32 v83, v85
	v_permlane32_swap_b32_e32 v86, v88
	v_permlane32_swap_b32_e32 v87, v89
	v_cmp_gt_f32_e32 vcc, 1.0, v90
	s_cbranch_vccz .LBB0_2121
	s_and_saveexec_b64 s[12:13], s[10:11]
	ds_write_b32 v196, v90 offset:128
	s_or_b64 exec, exec, s[12:13]
	s_waitcnt lgkmcnt(0)
	ds_read_b128 v[94:97], v221 offset:224
	ds_read_b128 v[98:101], v221 offset:192
	ds_read_b128 v[102:105], v221 offset:160
	ds_read_b128 v[106:109], v221 offset:128
	s_waitcnt lgkmcnt(3)
	v_pk_mul_f32 v[78:79], v[78:79], v[96:97]
	s_waitcnt lgkmcnt(2)
	v_pk_mul_f32 v[74:75], v[74:75], v[100:101]
	s_waitcnt lgkmcnt(1)
	v_pk_mul_f32 v[70:71], v[70:71], v[104:105]
	s_waitcnt lgkmcnt(0)
	v_pk_mul_f32 v[66:67], v[66:67], v[108:109]
	v_pk_mul_f32 v[76:77], v[76:77], v[94:95]
	v_pk_mul_f32 v[72:73], v[72:73], v[98:99]
	v_pk_mul_f32 v[68:69], v[68:69], v[102:103]
	v_pk_mul_f32 v[64:65], v[64:65], v[106:107]
	v_pk_mul_f32 v[62:63], v[62:63], v[96:97]
	v_pk_mul_f32 v[58:59], v[58:59], v[100:101]
	v_pk_mul_f32 v[54:55], v[54:55], v[104:105]
	v_pk_mul_f32 v[50:51], v[50:51], v[108:109]
	v_pk_mul_f32 v[60:61], v[60:61], v[94:95]
	v_pk_mul_f32 v[56:57], v[56:57], v[98:99]
	v_pk_mul_f32 v[52:53], v[52:53], v[102:103]
	v_pk_mul_f32 v[48:49], v[48:49], v[106:107]
	v_pk_mul_f32 v[46:47], v[46:47], v[96:97]
	v_pk_mul_f32 v[42:43], v[42:43], v[100:101]
	v_pk_mul_f32 v[38:39], v[38:39], v[104:105]
	v_pk_mul_f32 v[34:35], v[34:35], v[108:109]
	v_pk_mul_f32 v[44:45], v[44:45], v[94:95]
	v_pk_mul_f32 v[40:41], v[40:41], v[98:99]
	v_pk_mul_f32 v[36:37], v[36:37], v[102:103]
	v_pk_mul_f32 v[32:33], v[32:33], v[106:107]
	v_pk_mul_f32 v[30:31], v[30:31], v[96:97]
	v_pk_mul_f32 v[26:27], v[26:27], v[100:101]
	v_pk_mul_f32 v[22:23], v[22:23], v[104:105]
	v_pk_mul_f32 v[18:19], v[18:19], v[108:109]
	v_pk_mul_f32 v[28:29], v[28:29], v[94:95]
	v_pk_mul_f32 v[24:25], v[24:25], v[98:99]
	v_pk_mul_f32 v[20:21], v[20:21], v[102:103]
	v_pk_mul_f32 v[16:17], v[16:17], v[106:107]
